# v6 plus wait placement in router LN loop, routed-copy prefetch, post and combine loops
# baseline (speedup 1.0000x reference)
.LBB0_1528:
	s_or_saveexec_b64 s[4:5], s[4:5]
	v_mov_b64_e32 v[0:1], s[34:35]
	s_xor_b64 exec, exec, s[4:5]
	s_cbranch_execz .LBB0_1532
	s_mov_b64 s[6:7], exec
	v_mbcnt_lo_u32_b32 v0, s6, 0
	v_readlane_b32 s8, v255, 4
	v_mbcnt_hi_u32_b32 v0, s7, v0
	v_readlane_b32 s9, v255, 5
	s_lshl_b32 s34, s8, 6
	v_cmp_eq_u32_e32 vcc, 0, v0
	s_and_saveexec_b64 s[8:9], vcc
	s_cbranch_execz .LBB0_1531
	s_lshl_b64 s[10:11], s[34:35], 2
	s_add_u32 s10, s48, s10
	s_addc_u32 s11, s49, s11
	s_bcnt1_i32_b64 s6, s[6:7]
	s_lshl_b32 s6, s6, 4
	v_mov_b32_e32 v1, s6
	v_mov_b32_e32 v2, 0x1c000
	global_atomic_add v1, v2, v1, s[10:11] sc0
.LBB0_1531:
	s_or_b64 exec, exec, s[8:9]
	s_waitcnt vmcnt(0)
	v_readfirstlane_b32 s6, v1
	s_nop 1
	v_lshl_add_u32 v0, v0, 4, s6
	v_readlane_b32 s6, v254, 59
	s_nop 1
	v_mov_b32_e32 v1, s6
	ds_write_b32 v1, v0
	v_mov_b64_e32 v[0:1], s[34:35]

.LBB0_1535:
	s_and_b32 s15, s14, 1
	s_lshl_b32 s8, s15, 2
	s_add_i32 s8, s8, 0
	s_add_i32 s8, s8, 0x20780
	v_mov_b32_e32 v6, s8
	s_waitcnt lgkmcnt(0)
	s_barrier
	ds_read_b32 v6, v6
	s_movk_i32 s17, 0x5fff
	s_mov_b64 s[8:9], -1
	s_waitcnt lgkmcnt(0)
	v_cmp_lt_i32_e32 vcc, s17, v6
	v_readfirstlane_b32 s16, v6
	v_readfirstlane_b32 s17, v0
	s_cbranch_vccnz .LBB0_1534
	s_and_saveexec_b64 s[8:9], s[38:39]
	s_cbranch_execz .LBB0_1538
	v_mov_b32_e32 v199, 16
	global_atomic_add v92, v[0:1], v199, off sc0
.LBB0_1538:
	s_or_b64 exec, exec, s[8:9]
	s_lshl_b32 s60, s82, 1
	s_add_i32 s16, s16, s60
	s_cmpk_gt_i32 s16, 0x5fff
	s_cbranch_scc1 .LBB0_1575
	v_lshrrev_b32_e32 v6, 3, v227
	v_and_b32_e32 v7, 7, v227
	s_cmpk_gt_i32 s16, 0x3fff
	s_cbranch_scc1 .Lcv_down
	s_ashr_i32 s8, s16, 9
	s_load_dwordx2 s[18:19], s[46:47], 0x128
	s_ashr_i32 s9, s8, 31
	s_add_u32 s8, s6, s8
	s_addc_u32 s9, s7, s9
	s_lshl_b64 s[20:21], s[8:9], 23
	s_lshl_b64 s[8:9], s[8:9], 21
	s_add_u32 s8, s12, s8
	s_addc_u32 s9, s13, s9
	s_lshl_b32 s60, s16, 1
	s_and_b32 s60, s60, 0x380
	s_lshl_b32 s61, s16, 5
	s_and_b32 s61, s61, 0x7e0
	s_movk_i32 s62, 0x2000
	s_mov_b32 s63, 13
	s_waitcnt lgkmcnt(0)
	s_add_u32 s20, s18, s20
	s_addc_u32 s21, s19, s21
	v_lshl_add_u32 v8, v7, 2, s61
	v_and_b32_e32 v9, 0x3ff, v8
	v_lshrrev_b32_e32 v10, 7, v9
	v_and_b32_e32 v9, 0x7f, v9
	v_lshl_add_u32 v9, v10, 8, v9
	v_lshrrev_b32_e32 v10, 10, v8
	v_lshl_add_u32 v9, v10, 7, v9
	s_branch .Lcv_common

.Lcv_common:
	v_lshl_add_u32 v8, v6, 4, s60
	v_lshl_add_u32 v10, v7, 2, s61
	v_lshlrev_b32_e32 v8, s63, v8
	v_lshl_add_u32 v11, v6, 4, s60
	v_lshl_add_u32 v8, v10, 2, v8
	v_lshl_add_u32 v9, v9, 10, v11
	v_add_u32_e32 v10, 0x8000, v9
	global_load_dwordx4 v[94:97], v8, s[20:21] nt
	global_load_dwordx4 v[30:33], v8, s[20:21] offset:128 nt
	s_add_u32 s20, s20, s62
	s_addc_u32 s21, s21, 0
	global_load_dwordx4 v[98:101], v8, s[20:21] nt
	global_load_dwordx4 v[34:37], v8, s[20:21] offset:128 nt
	s_add_u32 s20, s20, s62
	s_addc_u32 s21, s21, 0
	global_load_dwordx4 v[102:105], v8, s[20:21] nt
	global_load_dwordx4 v[38:41], v8, s[20:21] offset:128 nt
	s_add_u32 s20, s20, s62
	s_addc_u32 s21, s21, 0
	global_load_dwordx4 v[106:109], v8, s[20:21] nt
	global_load_dwordx4 v[42:45], v8, s[20:21] offset:128 nt
	s_add_u32 s20, s20, s62
	s_addc_u32 s21, s21, 0
	global_load_dwordx4 v[110:113], v8, s[20:21] nt
	global_load_dwordx4 v[46:49], v8, s[20:21] offset:128 nt
	s_add_u32 s20, s20, s62
	s_addc_u32 s21, s21, 0
	global_load_dwordx4 v[114:117], v8, s[20:21] nt
	global_load_dwordx4 v[50:53], v8, s[20:21] offset:128 nt
	s_add_u32 s20, s20, s62
	s_addc_u32 s21, s21, 0
	global_load_dwordx4 v[118:121], v8, s[20:21] nt
	global_load_dwordx4 v[54:57], v8, s[20:21] offset:128 nt
	s_add_u32 s20, s20, s62
	s_addc_u32 s21, s21, 0
	global_load_dwordx4 v[122:125], v8, s[20:21] nt
	global_load_dwordx4 v[58:61], v8, s[20:21] offset:128 nt
	s_add_u32 s20, s20, s62
	s_addc_u32 s21, s21, 0
	global_load_dwordx4 v[126:129], v8, s[20:21] nt
	global_load_dwordx4 v[66:69], v8, s[20:21] offset:128 nt
	s_add_u32 s20, s20, s62
	s_addc_u32 s21, s21, 0
	global_load_dwordx4 v[130:133], v8, s[20:21] nt
	global_load_dwordx4 v[70:73], v8, s[20:21] offset:128 nt
	s_add_u32 s20, s20, s62
	s_addc_u32 s21, s21, 0
	global_load_dwordx4 v[134:137], v8, s[20:21] nt
	global_load_dwordx4 v[74:77], v8, s[20:21] offset:128 nt
	s_add_u32 s20, s20, s62
	s_addc_u32 s21, s21, 0
	global_load_dwordx4 v[138:141], v8, s[20:21] nt
	global_load_dwordx4 v[78:81], v8, s[20:21] offset:128 nt
	s_add_u32 s20, s20, s62
	s_addc_u32 s21, s21, 0
	global_load_dwordx4 v[142:145], v8, s[20:21] nt
	global_load_dwordx4 v[82:85], v8, s[20:21] offset:128 nt
	s_add_u32 s20, s20, s62
	s_addc_u32 s21, s21, 0
	global_load_dwordx4 v[146:149], v8, s[20:21] nt
	global_load_dwordx4 v[86:89], v8, s[20:21] offset:128 nt
	s_add_u32 s20, s20, s62
	s_addc_u32 s21, s21, 0
	global_load_dwordx4 v[150:153], v8, s[20:21] nt
	global_load_dwordx4 v[174:177], v8, s[20:21] offset:128 nt
	s_add_u32 s20, s20, s62
	s_addc_u32 s21, s21, 0
	global_load_dwordx4 v[154:157], v8, s[20:21] nt
	global_load_dwordx4 v[178:181], v8, s[20:21] offset:128 nt
	v_mov_b32_e32 v28, 0x42800000
	v_mov_b32_e32 v29, 0x42800000
	s_waitcnt vmcnt(30)
	v_pk_mul_f32 v[94:95], v[94:95], v[28:29]
	v_pk_mul_f32 v[96:97], v[96:97], v[28:29]
	v_pk_mul_f32 v[30:31], v[30:31], v[28:29]
	v_pk_mul_f32 v[32:33], v[32:33], v[28:29]
	s_waitcnt vmcnt(28)
	v_pk_mul_f32 v[98:99], v[98:99], v[28:29]
	v_pk_mul_f32 v[100:101], v[100:101], v[28:29]
	v_pk_mul_f32 v[34:35], v[34:35], v[28:29]
	v_pk_mul_f32 v[36:37], v[36:37], v[28:29]
	s_waitcnt vmcnt(26)
	v_pk_mul_f32 v[102:103], v[102:103], v[28:29]
	v_pk_mul_f32 v[104:105], v[104:105], v[28:29]
	v_pk_mul_f32 v[38:39], v[38:39], v[28:29]
	v_pk_mul_f32 v[40:41], v[40:41], v[28:29]
	s_waitcnt vmcnt(24)
	v_pk_mul_f32 v[106:107], v[106:107], v[28:29]
	v_pk_mul_f32 v[108:109], v[108:109], v[28:29]
	v_pk_mul_f32 v[42:43], v[42:43], v[28:29]
	v_pk_mul_f32 v[44:45], v[44:45], v[28:29]
	s_waitcnt vmcnt(22)
	v_pk_mul_f32 v[110:111], v[110:111], v[28:29]
	v_pk_mul_f32 v[112:113], v[112:113], v[28:29]
	v_pk_mul_f32 v[46:47], v[46:47], v[28:29]
	v_pk_mul_f32 v[48:49], v[48:49], v[28:29]
	s_waitcnt vmcnt(20)
	v_pk_mul_f32 v[114:115], v[114:115], v[28:29]
	v_pk_mul_f32 v[116:117], v[116:117], v[28:29]
	v_pk_mul_f32 v[50:51], v[50:51], v[28:29]
	v_pk_mul_f32 v[52:53], v[52:53], v[28:29]
	s_waitcnt vmcnt(18)
	v_pk_mul_f32 v[118:119], v[118:119], v[28:29]
	v_pk_mul_f32 v[120:121], v[120:121], v[28:29]
	v_pk_mul_f32 v[54:55], v[54:55], v[28:29]
	v_pk_mul_f32 v[56:57], v[56:57], v[28:29]
	s_waitcnt vmcnt(16)
	v_pk_mul_f32 v[122:123], v[122:123], v[28:29]
	v_pk_mul_f32 v[124:125], v[124:125], v[28:29]
	v_pk_mul_f32 v[58:59], v[58:59], v[28:29]
	v_pk_mul_f32 v[60:61], v[60:61], v[28:29]
	s_waitcnt vmcnt(14)
	v_pk_mul_f32 v[126:127], v[126:127], v[28:29]
	v_pk_mul_f32 v[128:129], v[128:129], v[28:29]
	v_pk_mul_f32 v[66:67], v[66:67], v[28:29]
	v_pk_mul_f32 v[68:69], v[68:69], v[28:29]
	s_waitcnt vmcnt(12)
	v_pk_mul_f32 v[130:131], v[130:131], v[28:29]
	v_pk_mul_f32 v[132:133], v[132:133], v[28:29]
	v_pk_mul_f32 v[70:71], v[70:71], v[28:29]
	v_pk_mul_f32 v[72:73], v[72:73], v[28:29]
	s_waitcnt vmcnt(10)
	v_pk_mul_f32 v[134:135], v[134:135], v[28:29]
	v_pk_mul_f32 v[136:137], v[136:137], v[28:29]
	v_pk_mul_f32 v[74:75], v[74:75], v[28:29]
	v_pk_mul_f32 v[76:77], v[76:77], v[28:29]
	s_waitcnt vmcnt(8)
	v_pk_mul_f32 v[138:139], v[138:139], v[28:29]
	v_pk_mul_f32 v[140:141], v[140:141], v[28:29]
	v_pk_mul_f32 v[78:79], v[78:79], v[28:29]
	v_pk_mul_f32 v[80:81], v[80:81], v[28:29]
	s_waitcnt vmcnt(6)
	v_pk_mul_f32 v[142:143], v[142:143], v[28:29]
	v_pk_mul_f32 v[144:145], v[144:145], v[28:29]
	v_pk_mul_f32 v[82:83], v[82:83], v[28:29]
	v_pk_mul_f32 v[84:85], v[84:85], v[28:29]
	s_waitcnt vmcnt(4)
	v_pk_mul_f32 v[146:147], v[146:147], v[28:29]
	v_pk_mul_f32 v[148:149], v[148:149], v[28:29]
	v_pk_mul_f32 v[86:87], v[86:87], v[28:29]
	v_pk_mul_f32 v[88:89], v[88:89], v[28:29]
	s_waitcnt vmcnt(2)
	v_pk_mul_f32 v[150:151], v[150:151], v[28:29]
	v_pk_mul_f32 v[152:153], v[152:153], v[28:29]
	v_pk_mul_f32 v[174:175], v[174:175], v[28:29]
	v_pk_mul_f32 v[176:177], v[176:177], v[28:29]
	s_waitcnt vmcnt(0)
	v_pk_mul_f32 v[154:155], v[154:155], v[28:29]
	v_pk_mul_f32 v[156:157], v[156:157], v[28:29]
	v_pk_mul_f32 v[178:179], v[178:179], v[28:29]
	v_pk_mul_f32 v[180:181], v[180:181], v[28:29]
	v_cvt_pk_fp8_f32 v12, v94, v98
	v_cvt_pk_fp8_f32 v13, v110, v114
	v_cvt_pk_fp8_f32 v14, v126, v130
	v_cvt_pk_fp8_f32 v15, v142, v146
	v_cvt_pk_fp8_f32 v16, v95, v99
	v_cvt_pk_fp8_f32 v17, v111, v115
	v_cvt_pk_fp8_f32 v18, v127, v131
	v_cvt_pk_fp8_f32 v19, v143, v147
	v_cvt_pk_fp8_f32 v20, v96, v100
	v_cvt_pk_fp8_f32 v21, v112, v116
	v_cvt_pk_fp8_f32 v22, v128, v132
	v_cvt_pk_fp8_f32 v23, v144, v148
	v_cvt_pk_fp8_f32 v24, v97, v101
	v_cvt_pk_fp8_f32 v25, v113, v117
	v_cvt_pk_fp8_f32 v26, v129, v133
	v_cvt_pk_fp8_f32 v27, v145, v149
	v_cvt_pk_fp8_f32 v12, v102, v106 op_sel:[0,0,1]
	v_cvt_pk_fp8_f32 v13, v118, v122 op_sel:[0,0,1]
	v_cvt_pk_fp8_f32 v14, v134, v138 op_sel:[0,0,1]
	v_cvt_pk_fp8_f32 v15, v150, v154 op_sel:[0,0,1]
	v_cvt_pk_fp8_f32 v16, v103, v107 op_sel:[0,0,1]
	v_cvt_pk_fp8_f32 v17, v119, v123 op_sel:[0,0,1]
	v_cvt_pk_fp8_f32 v18, v135, v139 op_sel:[0,0,1]
	v_cvt_pk_fp8_f32 v19, v151, v155 op_sel:[0,0,1]
	v_cvt_pk_fp8_f32 v20, v104, v108 op_sel:[0,0,1]
	v_cvt_pk_fp8_f32 v21, v120, v124 op_sel:[0,0,1]
	v_cvt_pk_fp8_f32 v22, v136, v140 op_sel:[0,0,1]
	v_cvt_pk_fp8_f32 v23, v152, v156 op_sel:[0,0,1]
	v_cvt_pk_fp8_f32 v24, v105, v109 op_sel:[0,0,1]
	v_cvt_pk_fp8_f32 v25, v121, v125 op_sel:[0,0,1]
	v_cvt_pk_fp8_f32 v26, v137, v141 op_sel:[0,0,1]
	v_cvt_pk_fp8_f32 v27, v153, v157 op_sel:[0,0,1]
	v_cvt_pk_fp8_f32 v182, v30, v34
	v_cvt_pk_fp8_f32 v183, v46, v50
	v_cvt_pk_fp8_f32 v184, v66, v70
	v_cvt_pk_fp8_f32 v185, v82, v86
	v_cvt_pk_fp8_f32 v186, v31, v35
	v_cvt_pk_fp8_f32 v187, v47, v51
	v_cvt_pk_fp8_f32 v188, v67, v71
	v_cvt_pk_fp8_f32 v189, v83, v87
	v_cvt_pk_fp8_f32 v190, v32, v36
	v_cvt_pk_fp8_f32 v191, v48, v52
	v_cvt_pk_fp8_f32 v192, v68, v72
	v_cvt_pk_fp8_f32 v193, v84, v88
	v_cvt_pk_fp8_f32 v194, v33, v37
	v_cvt_pk_fp8_f32 v195, v49, v53
	v_cvt_pk_fp8_f32 v196, v69, v73
	v_cvt_pk_fp8_f32 v197, v85, v89
	v_cvt_pk_fp8_f32 v182, v38, v42 op_sel:[0,0,1]
	v_cvt_pk_fp8_f32 v183, v54, v58 op_sel:[0,0,1]
	v_cvt_pk_fp8_f32 v184, v74, v78 op_sel:[0,0,1]
	v_cvt_pk_fp8_f32 v185, v174, v178 op_sel:[0,0,1]
	v_cvt_pk_fp8_f32 v186, v39, v43 op_sel:[0,0,1]
	v_cvt_pk_fp8_f32 v187, v55, v59 op_sel:[0,0,1]
	v_cvt_pk_fp8_f32 v188, v75, v79 op_sel:[0,0,1]
	v_cvt_pk_fp8_f32 v189, v175, v179 op_sel:[0,0,1]
	v_cvt_pk_fp8_f32 v190, v40, v44 op_sel:[0,0,1]
	v_cvt_pk_fp8_f32 v191, v56, v60 op_sel:[0,0,1]
	v_cvt_pk_fp8_f32 v192, v76, v80 op_sel:[0,0,1]
	v_cvt_pk_fp8_f32 v193, v176, v180 op_sel:[0,0,1]
	v_cvt_pk_fp8_f32 v194, v41, v45 op_sel:[0,0,1]
	v_cvt_pk_fp8_f32 v195, v57, v61 op_sel:[0,0,1]
	v_cvt_pk_fp8_f32 v196, v77, v81 op_sel:[0,0,1]
	v_cvt_pk_fp8_f32 v197, v177, v181 op_sel:[0,0,1]
	s_nop 1
	global_store_dwordx4 v9, v[12:15], s[8:9] nt
	global_store_dwordx4 v9, v[16:19], s[8:9] offset:1024 nt
	global_store_dwordx4 v9, v[20:23], s[8:9] offset:2048 nt
	global_store_dwordx4 v9, v[24:27], s[8:9] offset:3072 nt
	global_store_dwordx4 v10, v[182:185], s[8:9] nt
	global_store_dwordx4 v10, v[186:189], s[8:9] offset:1024 nt
	global_store_dwordx4 v10, v[190:193], s[8:9] offset:2048 nt
	global_store_dwordx4 v10, v[194:197], s[8:9] offset:3072 nt
	s_and_saveexec_b64 s[8:9], s[38:39]
	s_cbranch_execz .LBB0_1533
	s_xor_b32 s15, s15, 1
	s_lshl_b32 s15, s15, 2
	s_add_i32 s15, s15, 0
	s_add_i32 s15, s15, 0x20780
	v_mov_b32_e32 v6, s15
	s_waitcnt vmcnt(8)
	ds_write_b32 v6, v92
	s_branch .LBB0_1533

.LBB0_1643:
	s_andn2_b64 vcc, exec, s[4:5]
	s_cbranch_vccnz .LBB0_1702
	s_lshl_b32 s26, s91, 3
	s_abs_i32 s4, s26
	s_waitcnt vmcnt(0)
	v_cvt_f32_u32_e32 v0, s4
	s_lshl_b32 s5, s93, 3
	s_add_i32 s22, s5, s82
	s_sub_i32 s5, s26, s22
	v_rcp_iflag_f32_e32 v0, v0
	s_add_i32 s7, s5, 0x3fff
	s_sub_i32 s5, 0xffffc001, s5
	s_xor_b32 s8, s7, s26
	v_mul_f32_e32 v0, 0x4f7ffffe, v0
	v_cvt_u32_f32_e32 v0, v0
	s_sub_i32 s6, 0, s4
	s_max_i32 s5, s7, s5
	s_ashr_i32 s7, s8, 31
	v_readfirstlane_b32 s8, v0
	s_mul_i32 s6, s6, s8
	s_mul_hi_u32 s6, s8, s6
	s_add_i32 s8, s8, s6
	s_mul_hi_u32 s6, s5, s8
	s_mul_i32 s8, s6, s4
	s_sub_i32 s5, s5, s8
	s_add_i32 s8, s6, 1
	s_sub_i32 s9, s5, s4
	s_cmp_ge_u32 s5, s4
	s_cselect_b32 s6, s8, s6
	s_cselect_b32 s5, s9, s5
	s_add_i32 s8, s6, 1
	s_cmp_ge_u32 s5, s4
	s_cselect_b32 s4, s8, s6
	s_xor_b32 s4, s4, s7
	s_sub_i32 s27, s4, s7
	s_cmp_lt_i32 s27, 1
	s_cbranch_scc1 .LBB0_1651
	s_load_dwordx2 s[18:19], s[16:17], 0x170
	s_load_dwordx2 s[24:25], s[16:17], 0xb8
	v_readlane_b32 s38, v255, 4
	v_readlane_b32 s39, v255, 5
	v_lshlrev_b32_e32 v90, 3, v32
	s_waitcnt lgkmcnt(0)
	s_add_u32 s33, s18, 0x48000000
	s_addc_u32 s40, s19, 0
	s_add_u32 s4, s18, 0x72200000
	s_addc_u32 s5, s19, 0
	s_add_u32 s6, s18, 0x74200000
	s_addc_u32 s7, s19, 0
	s_add_u32 s8, s18, 0x76200000
	s_addc_u32 s9, s19, 0
	s_add_u32 s10, s18, 0x78200000
	s_addc_u32 s11, s19, 0
	s_add_u32 s12, s18, 0x63000000
	s_addc_u32 s13, s19, 0
	s_add_u32 s14, s18, 0x60000000
	s_addc_u32 s15, s19, 0
	s_add_u32 s20, s18, 0x6c000000
	s_addc_u32 s21, s19, 0
	s_lshl_b32 s34, s38, 9
	s_lshl_b64 s[38:39], s[34:35], 2
	v_ashrrev_i32_e32 v91, 31, v90
	s_add_u32 s24, s24, s38
	s_addc_u32 s25, s25, s39
	v_lshlrev_b64 v[24:25], 2, v[90:91]
	v_lshl_add_u64 v[4:5], s[24:25], 0, v[24:25]
	global_load_dwordx4 v[0:3], v[4:5], off
	s_nop 0
	global_load_dwordx4 v[4:7], v[4:5], off offset:16
	s_load_dwordx4 s[44:47], s[16:17], 0x78
	s_nop 0
	s_load_dwordx2 s[16:17], s[16:17], 0x90
	v_ashrrev_i32_e32 v32, 3, v32
	v_ashrrev_i32_e32 v33, 31, v32
	v_lshlrev_b64 v[32:33], 2, v[32:33]
	s_mov_b32 s34, 0
	s_waitcnt lgkmcnt(0)
	s_add_u32 s16, s16, s38
	s_addc_u32 s17, s17, s39
	v_lshl_add_u64 v[12:13], s[16:17], 0, v[24:25]
	s_add_u32 s16, s46, s38
	s_addc_u32 s17, s47, s39
	v_lshl_add_u64 v[20:21], s[16:17], 0, v[24:25]
	s_add_u32 s16, s44, s38
	s_addc_u32 s17, s45, s39
	s_ashr_i32 s23, s22, 31
	v_lshl_add_u64 v[28:29], s[16:17], 0, v[24:25]
	s_lshl_b64 s[16:17], s[22:23], 5
	s_add_u32 s16, s20, s16
	s_addc_u32 s17, s21, s17
	v_lshl_add_u64 v[34:35], s[16:17], 0, v[32:33]
	s_mul_i32 s16, s22, 0x5800
	s_mul_hi_i32 s17, s22, 0x5800
	s_add_u32 s16, s33, s16
	s_addc_u32 s17, s40, s17
	global_load_dwordx4 v[8:11], v[12:13], off
	s_nop 0
	global_load_dwordx4 v[12:15], v[12:13], off offset:16
	s_nop 0
	global_load_dwordx4 v[16:19], v[20:21], off
	s_nop 0
	global_load_dwordx4 v[20:23], v[20:21], off offset:16
	s_nop 0
	global_load_dwordx4 v[24:27], v[28:29], off
	s_nop 0
	global_load_dwordx4 v[28:31], v[28:29], off offset:16
	v_lshl_add_u64 v[94:95], s[20:21], 0, v[32:33]
	global_load_dword v92, v[34:35], off
	v_lshl_add_u64 v[34:35], v[90:91], 1, s[16:17]
	s_movk_i32 s16, 0x2000
	v_add_co_u32_e32 v36, vcc, s16, v34
	s_movk_i32 s16, 0x1000
	s_nop 0
	v_addc_co_u32_e32 v37, vcc, 0, v35, vcc
	v_add_co_u32_e32 v34, vcc, s16, v34
	s_lshl_b64 s[16:17], s[22:23], 9
	s_nop 0
	v_addc_co_u32_e32 v35, vcc, 0, v35, vcc
	global_load_dwordx4 v[60:63], v[36:37], off offset:2560
	global_load_dwordx4 v[70:73], v[34:35], off offset:2560
	v_lshl_add_u64 v[34:35], s[16:17], 0, v[90:91]
	v_lshlrev_b64 v[34:35], 1, v[34:35]
	v_lshl_add_u64 v[36:37], s[14:15], 0, v[34:35]
	global_load_dwordx4 v[78:81], v[36:37], off
	v_lshl_add_u64 v[36:37], s[12:13], 0, v[34:35]
	global_load_dwordx4 v[82:85], v[36:37], off
	v_lshl_add_u64 v[36:37], s[8:9], 0, v[34:35]
	global_load_dwordx4 v[66:69], v[36:37], off nt
	v_lshl_add_u64 v[36:37], s[6:7], 0, v[34:35]
	v_lshl_add_u64 v[34:35], s[4:5], 0, v[34:35]
	global_load_dwordx4 v[74:77], v[36:37], off nt
	global_load_dwordx4 v[86:89], v[34:35], off nt
	s_add_u32 s16, s18, 0x78a00000
	s_addc_u32 s17, s19, 0
	s_add_u32 s18, s18, 0x79200000
	s_addc_u32 s19, s19, 0
	s_waitcnt vmcnt(0)
	v_mov_b32_e32 v101, v26
	s_waitcnt vmcnt(8)
	v_mov_b32_e32 v97, v30
	v_mov_b32_e32 v99, v28
	v_mov_b32_e32 v93, v24
	s_branch .LBB0_1647
.LBB0_1646:
	s_nop 0
	v_lshlrev_b32_e32 v106, 16, v86
	v_and_b32_e32 v107, 0xffff0000, v86
	v_add_f32_e32 v24, 0, v106
	v_and_b32_e32 v102, 0xffff0000, v89
	v_lshlrev_b32_e32 v103, 16, v89
	v_lshlrev_b32_e32 v89, 16, v87
	v_add_f32_e32 v24, v24, v107
	v_and_b32_e32 v104, 0xffff0000, v88
	v_lshlrev_b32_e32 v105, 16, v88
	v_and_b32_e32 v88, 0xffff0000, v87
	v_add_f32_e32 v24, v24, v89
	v_add_f32_e32 v24, v24, v88
	v_add_f32_e32 v24, v24, v105
	v_add_f32_e32 v24, v24, v104
	v_add_f32_e32 v24, v24, v103
	v_add_f32_e32 v24, v24, v102
	v_lshlrev_b32_e32 v28, 16, v83
	v_and_b32_e32 v96, 0xffff0000, v83
	v_add_f32_dpp v24, v24, v24 quad_perm:[1,0,3,2] row_mask:0xf bank_mask:0xf bound_ctrl:1
	v_lshlrev_b32_e32 v114, 16, v85
	v_and_b32_e32 v115, 0xffff0000, v85
	v_add_f32_dpp v24, v24, v24 quad_perm:[2,3,0,1] row_mask:0xf bank_mask:0xf bound_ctrl:1
	v_mov_b32_e32 v100, v92
	v_mov_b32_e32 v98, v92
	v_add_f32_dpp v24, v24, v24 row_half_mirror row_mask:0xf bank_mask:0xf bound_ctrl:1
	v_mul_f32_e32 v24, 0x3c800000, v24
	v_pk_add_f32 v[86:87], v[106:107], v[24:25] op_sel_hi:[1,0] neg_lo:[0,1] neg_hi:[0,1]
	v_pk_add_f32 v[88:89], v[88:89], v[24:25] op_sel_hi:[1,0] neg_lo:[0,1] neg_hi:[0,1]
	v_pk_mul_f32 v[106:107], v[86:87], v[86:87]
	v_pk_mul_f32 v[108:109], v[88:89], v[88:89]
	v_pk_add_f32 v[104:105], v[104:105], v[24:25] op_sel_hi:[1,0] neg_lo:[0,1] neg_hi:[0,1]
	v_pk_add_f32 v[102:103], v[102:103], v[24:25] op_sel_hi:[1,0] neg_lo:[0,1] neg_hi:[0,1]
	v_add_f32_e32 v24, v106, v107
	v_add_f32_e32 v24, v109, v24
	v_pk_mul_f32 v[110:111], v[104:105], v[104:105]
	v_add_f32_e32 v24, v108, v24
	v_add_f32_e32 v24, v111, v24
	v_pk_mul_f32 v[112:113], v[102:103], v[102:103]
	v_add_f32_e32 v24, v110, v24
	v_add_f32_e32 v24, v113, v24
	v_add_f32_e32 v24, v112, v24
	v_lshlrev_b32_e32 v111, 16, v84
	v_and_b32_e32 v113, 0xffff0000, v84
	v_add_f32_dpp v24, v24, v24 quad_perm:[1,0,3,2] row_mask:0xf bank_mask:0xf bound_ctrl:1
	v_lshlrev_b32_e32 v84, 16, v79
	v_and_b32_e32 v106, 0xffff0000, v79
	v_add_f32_dpp v24, v24, v24 quad_perm:[2,3,0,1] row_mask:0xf bank_mask:0xf bound_ctrl:1
	v_lshlrev_b32_e32 v108, 16, v80
	v_and_b32_e32 v80, 0xffff0000, v80
	v_add_f32_dpp v24, v24, v24 row_half_mirror row_mask:0xf bank_mask:0xf bound_ctrl:1
	v_fmamk_f32 v24, v24, 0x3c800000, v217
	v_cmp_gt_f32_e32 vcc, s28, v24
	v_mul_f32_e32 v26, 0x4b800000, v24
	v_lshlrev_b32_e32 v110, 16, v81
	v_cndmask_b32_e32 v24, v24, v26, vcc
	v_rsq_f32_e32 v24, v24
	v_and_b32_e32 v112, 0xffff0000, v81
	s_ashr_i32 s23, s22, 31
	s_lshl_b64 s[22:23], s[22:23], 9
	v_mul_f32_e32 v26, 0x45800000, v24
	v_cndmask_b32_e32 v30, v24, v26, vcc
	v_lshlrev_b32_e32 v24, 16, v82
	v_and_b32_e32 v26, 0xffff0000, v82
	v_lshlrev_b32_e32 v82, 16, v78
	v_mul_f32_e32 v83, v86, v30
	v_pk_mul_f32 v[82:83], v[92:93], v[82:83]
	v_and_b32_e32 v78, 0xffff0000, v78
	v_add_f32_e32 v79, v16, v83
	v_add_f32_e32 v79, v82, v79
	v_mul_f32_e32 v82, v79, v24
	v_mul_f32_e32 v79, v87, v30
	v_mov_b32_e32 v24, v92
	v_pk_mul_f32 v[78:79], v[24:25], v[78:79]
	v_mul_f32_e32 v85, v89, v30
	v_add_f32_e32 v24, v17, v79
	v_add_f32_e32 v24, v78, v24
	v_pk_mul_f32 v[78:79], v[100:101], v[84:85]
	v_mul_f32_e32 v24, v24, v26
	v_add_f32_e32 v26, v18, v79
	v_add_f32_e32 v26, v78, v26
	v_mul_f32_e32 v83, v26, v28
	v_mul_f32_e32 v107, v88, v30
	v_mov_b32_e32 v26, v92
	v_pk_mul_f32 v[78:79], v[26:27], v[106:107]
	v_mul_f32_e32 v109, v105, v30
	v_add_f32_e32 v26, v19, v79
	v_add_f32_e32 v26, v78, v26
	v_pk_mul_f32 v[78:79], v[98:99], v[108:109]
	v_mul_f32_e32 v81, v104, v30
	v_add_f32_e32 v28, v20, v79
	v_add_f32_e32 v28, v78, v28
	v_mul_f32_e32 v84, v28, v111
	v_mov_b32_e32 v28, v92
	v_pk_mul_f32 v[78:79], v[28:29], v[80:81]
	v_mul_f32_e32 v80, 0x41000000, v82
	v_mul_f32_e32 v24, 0x41000000, v24
	v_med3_f32 v81, v80, s3, v225
	v_med3_f32 v24, v24, s3, v225
	v_mov_b32_e32 v80, v65
	v_mul_f32_e32 v26, v26, v96
	v_add_f32_e32 v28, v21, v79
	v_mul_f32_e32 v111, v103, v30
	v_mov_b32_e32 v96, v92
	v_cvt_pk_fp8_f32 v80, v81, v24
	v_add_f32_e32 v28, v78, v28
	v_pk_mul_f32 v[78:79], v[96:97], v[110:111]
	v_mul_f32_e32 v24, 0x41000000, v83
	v_add_f32_e32 v79, v22, v79
	v_mul_f32_e32 v26, 0x41000000, v26
	v_mul_f32_e32 v28, v28, v113
	v_add_f32_e32 v78, v78, v79
	v_mul_f32_e32 v113, v102, v30
	v_mov_b32_e32 v30, v92
	v_med3_f32 v24, v24, s3, v225
	v_med3_f32 v26, v26, s3, v225
	v_mul_f32_e32 v85, v78, v114
	v_pk_mul_f32 v[78:79], v[30:31], v[112:113]
	v_cvt_pk_fp8_f32 v80, v24, v26 op_sel:[0,0,1]
	v_mul_f32_e32 v24, 0x41000000, v84
	v_mul_f32_e32 v26, 0x41000000, v28
	v_add_f32_e32 v30, v23, v79
	v_med3_f32 v24, v24, s3, v225
	v_med3_f32 v26, v26, s3, v225
	v_mov_b32_e32 v81, v65
	v_add_f32_e32 v30, v78, v30
	v_cvt_pk_fp8_f32 v81, v24, v26
	v_mul_f32_e32 v30, v30, v115
	v_mul_f32_e32 v24, 0x41000000, v85
	v_mul_f32_e32 v26, 0x41000000, v30
	v_med3_f32 v24, v24, s3, v225
	v_med3_f32 v26, v26, s3, v225
	v_cvt_pk_fp8_f32 v81, v24, v26 op_sel:[0,0,1]
	v_lshl_add_u64 v[78:79], s[22:23], 0, v[90:91]
	v_lshl_add_u64 v[82:83], s[10:11], 0, v[78:79]
	v_lshlrev_b32_e32 v102, 16, v71
	global_store_dwordx2 v[82:83], v[80:81], off
	v_lshlrev_b32_e32 v80, 16, v73
	v_mul_f32_e32 v24, 0xbfb8aa3b, v80
	v_exp_f32_e32 v24, v24
	v_lshlrev_b32_e32 v81, 16, v77
	v_and_b32_e32 v83, 0xffff0000, v77
	v_mov_b32_e32 v86, v83
	v_mov_b32_e32 v87, v81
	v_add_f32_e32 v24, 1.0, v24
	v_pk_mul_f32 v[104:105], v[86:87], v[86:87]
	v_lshlrev_b32_e32 v86, 16, v72
	v_rcp_f32_e32 v84, v24
	v_mul_f32_e32 v24, 0xbfb8aa3b, v86
	v_exp_f32_e32 v24, v24
	v_and_b32_e32 v72, 0xffff0000, v72
	v_and_b32_e32 v82, 0xffff0000, v73
	v_lshlrev_b32_e32 v87, 16, v76
	v_add_f32_e32 v24, 1.0, v24
	v_rcp_f32_e32 v88, v24
	v_mul_f32_e32 v24, 0xbfb8aa3b, v72
	v_exp_f32_e32 v24, v24
	v_and_b32_e32 v73, 0xffff0000, v76
	v_mov_b32_e32 v76, v73
	v_mov_b32_e32 v77, v87
	v_add_f32_e32 v24, 1.0, v24
	v_pk_mul_f32 v[106:107], v[76:77], v[76:77]
	v_rcp_f32_e32 v76, v24
	v_mul_f32_e32 v24, 0xbfb8aa3b, v102
	v_exp_f32_e32 v24, v24
	v_and_b32_e32 v110, 0xffff0000, v71
	v_lshlrev_b32_e32 v116, 16, v70
	v_lshlrev_b32_e32 v103, 16, v75
	v_add_f32_e32 v24, 1.0, v24
	v_rcp_f32_e32 v108, v24
	v_mul_f32_e32 v24, 0xbfb8aa3b, v110
	v_exp_f32_e32 v24, v24
	v_and_b32_e32 v111, 0xffff0000, v75
	v_lshlrev_b32_e32 v117, 16, v74
	v_and_b32_e32 v75, 0xffff0000, v74
	v_add_f32_e32 v24, 1.0, v24
	v_rcp_f32_e32 v114, v24
	v_mul_f32_e32 v24, 0xbfb8aa3b, v116
	v_exp_f32_e32 v24, v24
	v_and_b32_e32 v74, 0xffff0000, v70
	v_lshlrev_b32_e32 v126, 16, v66
	v_and_b32_e32 v128, 0xffff0000, v66
	v_add_f32_e32 v24, 1.0, v24
	v_rcp_f32_e32 v118, v24
	v_mul_f32_e32 v24, 0xbfb8aa3b, v74
	v_exp_f32_e32 v24, v24
	v_and_b32_e32 v66, 0xffff0000, v67
	v_lshlrev_b32_e32 v67, 16, v67
	v_lshlrev_b32_e32 v133, 16, v68
	v_add_f32_e32 v24, 1.0, v24
	v_rcp_f32_e32 v120, v24
	v_mul_f32_e32 v24, 0xbfb8aa3b, v82
	v_exp_f32_e32 v24, v24
	v_and_b32_e32 v132, 0xffff0000, v68
	v_lshlrev_b32_e32 v131, 16, v69
	v_and_b32_e32 v130, 0xffff0000, v69
	v_add_f32_e32 v24, 1.0, v24
	v_rcp_f32_e32 v122, v24
	v_add_f32_e32 v24, 0, v126
	v_add_f32_e32 v24, v24, v128
	v_add_f32_e32 v24, v24, v67
	v_add_f32_e32 v24, v24, v66
	v_add_f32_e32 v24, v24, v133
	v_add_f32_e32 v24, v24, v132
	v_add_f32_e32 v24, v24, v131
	v_add_f32_e32 v24, v24, v130
	v_mov_b32_e32 v112, v111
	v_mov_b32_e32 v113, v103
	v_add_f32_dpp v24, v24, v24 quad_perm:[1,0,3,2] row_mask:0xf bank_mask:0xf bound_ctrl:1
	v_mov_b32_e32 v129, v75
	v_pk_mul_f32 v[112:113], v[112:113], v[112:113]
	v_add_f32_dpp v24, v24, v24 quad_perm:[2,3,0,1] row_mask:0xf bank_mask:0xf bound_ctrl:1
	v_mov_b32_e32 v127, v117
	v_mov_b32_e32 v69, v113
	v_add_f32_dpp v24, v24, v24 row_half_mirror row_mask:0xf bank_mask:0xf bound_ctrl:1
	s_brev_b32 s22, 60
	v_lshl_add_u64 v[124:125], s[16:17], 0, v[78:79]
	v_add_f32_dpp v26, v24, v24 row_ror:8 row_mask:0xf bank_mask:0xf bound_ctrl:1
	v_mul_f32_e32 v24, 0x3c000000, v26
	v_fmac_f32_e32 v128, 0xbc000000, v26
	v_pk_add_f32 v[70:71], v[66:67], v[24:25] op_sel_hi:[1,0] neg_lo:[0,1] neg_hi:[0,1]
	v_fmac_f32_e32 v126, 0xbc000000, v26
	v_pk_mul_f32 v[134:135], v[70:71], v[70:71]
	v_pk_mul_f32 v[66:67], v[128:129], v[128:129]
	v_mov_b32_e32 v68, v135
	v_pk_fma_f32 v[66:67], v[126:127], v[126:127], v[66:67]
	v_mov_b32_e32 v135, v112
	v_pk_add_f32 v[136:137], v[68:69], v[66:67]
	v_pk_add_f32 v[68:69], v[132:133], v[24:25] op_sel_hi:[1,0] neg_lo:[0,1] neg_hi:[0,1]
	v_pk_add_f32 v[66:67], v[130:131], v[24:25] op_sel_hi:[1,0] neg_lo:[0,1] neg_hi:[0,1]
	v_pk_mul_f32 v[132:133], v[68:69], v[68:69]
	v_pk_add_f32 v[112:113], v[134:135], v[136:137]
	v_mov_b32_e32 v134, v133
	v_mov_b32_e32 v135, v107
	v_pk_mul_f32 v[130:131], v[66:67], v[66:67]
	v_pk_add_f32 v[112:113], v[134:135], v[112:113]
	v_mov_b32_e32 v133, v106
	v_pk_add_f32 v[106:107], v[132:133], v[112:113]
	v_mov_b32_e32 v112, v131
	v_mov_b32_e32 v113, v105
	v_pk_add_f32 v[106:107], v[112:113], v[106:107]
	v_mov_b32_e32 v131, v104
	v_pk_add_f32 v[104:105], v[130:131], v[106:107]
	s_cmp_lg_u32 s27, s34
	s_nop 0
	v_mov_b32_dpp v107, v105 quad_perm:[1,0,3,2] row_mask:0xf bank_mask:0xf bound_ctrl:1
	v_mov_b32_dpp v106, v104 quad_perm:[1,0,3,2] row_mask:0xf bank_mask:0xf bound_ctrl:1
	v_pk_add_f32 v[104:105], v[104:105], v[106:107]
	s_nop 1
	v_mov_b32_dpp v107, v105 quad_perm:[2,3,0,1] row_mask:0xf bank_mask:0xf bound_ctrl:1
	v_mov_b32_dpp v106, v104 quad_perm:[2,3,0,1] row_mask:0xf bank_mask:0xf bound_ctrl:1
	v_pk_add_f32 v[104:105], v[104:105], v[106:107]
	s_nop 1
	v_mov_b32_dpp v107, v105 row_half_mirror row_mask:0xf bank_mask:0xf bound_ctrl:1
	v_mov_b32_dpp v106, v104 row_half_mirror row_mask:0xf bank_mask:0xf bound_ctrl:1
	v_pk_add_f32 v[104:105], v[104:105], v[106:107]
	s_nop 1
	v_mov_b32_dpp v107, v105 row_ror:8 row_mask:0xf bank_mask:0xf bound_ctrl:1
	v_mov_b32_dpp v106, v104 row_ror:8 row_mask:0xf bank_mask:0xf bound_ctrl:1
	v_pk_add_f32 v[104:105], v[104:105], v[106:107]
	s_nop 0
	v_pk_fma_f32 v[104:105], v[104:105], s[22:23], v[166:167] op_sel_hi:[1,0,0]
	s_mov_b32 s22, s20
	v_mul_f32_e32 v24, 0x4b800000, v105
	v_cmp_gt_f32_e64 s[38:39], s28, v105
	v_cmp_gt_f32_e32 vcc, s28, v104
	s_nop 0
	v_cndmask_b32_e64 v24, v105, v24, s[38:39]
	v_rsq_f32_e32 v24, v24
	s_nop 0
	v_mul_f32_e32 v26, 0x45800000, v24
	v_cndmask_b32_e64 v119, v24, v26, s[38:39]
	v_mov_b32_e32 v121, v119
	v_pk_mul_f32 v[74:75], v[120:121], v[74:75]
	v_mov_b32_e32 v109, v119
	v_mul_f32_e32 v26, v9, v75
	v_mul_f32_e32 v26, v74, v26
	v_pk_mul_f32 v[74:75], v[108:109], v[102:103]
	v_mov_b32_e32 v115, v119
	v_mul_f32_e32 v28, v10, v75
	v_mul_f32_e32 v28, v74, v28
	v_pk_mul_f32 v[74:75], v[114:115], v[110:111]
	v_mov_b32_e32 v89, v119
	v_mul_f32_e32 v30, v11, v75
	v_mov_b32_e32 v77, v119
	v_mul_f32_e32 v30, v74, v30
	v_pk_mul_f32 v[74:75], v[88:89], v[86:87]
	v_pk_mul_f32 v[72:73], v[76:77], v[72:73]
	v_mul_f32_e32 v75, v12, v75
	v_mul_f32_e32 v73, v13, v73
	v_mov_b32_e32 v85, v119
	v_pk_mul_f32 v[106:107], v[118:119], v[116:117]
	v_mul_f32_e32 v74, v74, v75
	v_mul_f32_e32 v75, v72, v73
	v_pk_mul_f32 v[72:73], v[84:85], v[80:81]
	v_mul_f32_e32 v24, v8, v107
	v_mul_f32_e32 v73, v14, v73
	v_mov_b32_e32 v123, v119
	v_mul_f32_e32 v24, v106, v24
	v_mul_f32_e32 v76, v72, v73
	v_pk_mul_f32 v[72:73], v[122:123], v[82:83]
	v_mul_f32_e32 v24, 0x41000000, v24
	v_mul_f32_e32 v73, v15, v73
	v_mul_f32_e32 v26, 0x41000000, v26
	v_mul_f32_e32 v77, v72, v73
	v_med3_f32 v24, v24, s3, v225
	v_med3_f32 v26, v26, s3, v225
	v_mov_b32_e32 v72, v65
	v_cvt_pk_fp8_f32 v72, v24, v26
	v_mul_f32_e32 v24, 0x41000000, v28
	v_mul_f32_e32 v26, 0x41000000, v30
	v_med3_f32 v24, v24, s3, v225
	v_med3_f32 v26, v26, s3, v225
	v_cvt_pk_fp8_f32 v72, v24, v26 op_sel:[0,0,1]
	v_mul_f32_e32 v24, 0x41000000, v74
	v_mul_f32_e32 v26, 0x41000000, v75
	v_med3_f32 v24, v24, s3, v225
	v_med3_f32 v26, v26, s3, v225
	v_mov_b32_e32 v73, v65
	v_cvt_pk_fp8_f32 v73, v24, v26
	v_mul_f32_e32 v24, 0x41000000, v76
	v_mul_f32_e32 v26, 0x41000000, v77
	v_med3_f32 v24, v24, s3, v225
	v_med3_f32 v26, v26, s3, v225
	v_cvt_pk_fp8_f32 v73, v24, v26 op_sel:[0,0,1]
	v_mul_f32_e32 v24, 0x4b800000, v104
	v_cndmask_b32_e32 v24, v104, v24, vcc
	v_rsq_f32_e32 v24, v24
	v_and_b32_e32 v28, 0xffff0000, v60
	v_lshlrev_b32_e32 v30, 16, v61
	global_store_dwordx2 v[124:125], v[72:73], off
	v_mul_f32_e32 v26, 0x45800000, v24
	v_cndmask_b32_e32 v24, v24, v26, vcc
	v_lshlrev_b32_e32 v26, 16, v60
	v_and_b32_e32 v60, 0xffff0000, v61
	v_mul_f32_e32 v60, 0xbfb8aa3b, v60
	v_lshlrev_b32_e32 v61, 16, v62
	v_exp_f32_e32 v60, v60
	v_mul_f32_e32 v61, 0xbfb8aa3b, v61
	v_and_b32_e32 v62, 0xffff0000, v62
	v_exp_f32_e32 v61, v61
	v_mul_f32_e32 v62, 0xbfb8aa3b, v62
	v_add_f32_e32 v60, 1.0, v60
	v_exp_f32_e32 v62, v62
	v_rcp_f32_e32 v60, v60
	v_add_f32_e32 v61, 1.0, v61
	v_mul_f32_e32 v70, v70, v24
	v_rcp_f32_e32 v61, v61
	v_mul_f32_e32 v70, v3, v70
	v_add_f32_e32 v62, 1.0, v62
	v_mul_f32_e32 v70, v60, v70
	v_mul_f32_e32 v60, v69, v24
	v_rcp_f32_e32 v62, v62
	v_mul_f32_e32 v60, v4, v60
	v_mul_f32_e32 v61, v61, v60
	v_mul_f32_e32 v60, v68, v24
	v_lshlrev_b32_e32 v72, 16, v63
	v_mul_f32_e32 v60, v5, v60
	v_mul_f32_e32 v62, v62, v60
	v_mul_f32_e32 v60, v67, v24
	v_mul_f32_e32 v67, 0xbfb8aa3b, v72
	v_exp_f32_e32 v67, v67
	v_mul_f32_e32 v26, 0xbfb8aa3b, v26
	v_exp_f32_e32 v26, v26
	v_mul_f32_e32 v28, 0xbfb8aa3b, v28
	v_add_f32_e32 v67, 1.0, v67
	v_rcp_f32_e32 v67, v67
	v_and_b32_e32 v63, 0xffff0000, v63
	v_exp_f32_e32 v28, v28
	v_mul_f32_e32 v60, v6, v60
	v_mul_f32_e32 v67, v67, v60
	v_mul_f32_e32 v60, 0xbfb8aa3b, v63
	v_add_f32_e32 v26, 1.0, v26
	v_exp_f32_e32 v60, v60
	v_rcp_f32_e32 v26, v26
	v_mul_f32_e32 v30, 0xbfb8aa3b, v30
	v_add_f32_e32 v28, 1.0, v28
	v_exp_f32_e32 v30, v30
	v_mul_f32_e32 v73, v126, v24
	v_rcp_f32_e32 v28, v28
	v_mul_f32_e32 v73, v0, v73
	v_add_f32_e32 v60, 1.0, v60
	v_mul_f32_e32 v26, v26, v73
	v_mul_f32_e32 v73, v128, v24
	v_rcp_f32_e32 v60, v60
	v_mul_f32_e32 v73, v1, v73
	v_add_f32_e32 v30, 1.0, v30
	v_mul_f32_e32 v28, v28, v73
	v_mul_f32_e32 v71, v71, v24
	v_rcp_f32_e32 v30, v30
	v_mul_f32_e32 v24, v66, v24
	v_mul_f32_e32 v24, v7, v24
	v_mul_f32_e32 v26, 0x41000000, v26
	v_mul_f32_e32 v28, 0x41000000, v28
	v_mul_f32_e32 v24, v60, v24
	v_med3_f32 v26, v26, s3, v225
	v_med3_f32 v28, v28, s3, v225
	v_mov_b32_e32 v60, v65
	v_mul_f32_e32 v71, v2, v71
	v_cvt_pk_fp8_f32 v60, v26, v28
	v_mul_f32_e32 v30, v30, v71
	v_mul_f32_e32 v26, 0x41000000, v30
	v_mul_f32_e32 v28, 0x41000000, v70
	v_med3_f32 v26, v26, s3, v225
	v_med3_f32 v28, v28, s3, v225
	v_cvt_pk_fp8_f32 v60, v26, v28 op_sel:[0,0,1]
	v_mul_f32_e32 v26, 0x41000000, v61
	v_mul_f32_e32 v28, 0x41000000, v62
	v_med3_f32 v26, v26, s3, v225
	v_med3_f32 v28, v28, s3, v225
	v_mov_b32_e32 v61, v65
	v_cvt_pk_fp8_f32 v61, v26, v28
	v_mul_f32_e32 v26, 0x41000000, v67
	v_mul_f32_e32 v24, 0x41000000, v24
	v_med3_f32 v26, v26, s3, v225
	v_med3_f32 v24, v24, s3, v225
	v_cvt_pk_fp8_f32 v61, v26, v24 op_sel:[0,0,1]
	v_lshl_add_u64 v[62:63], s[18:19], 0, v[78:79]
	s_waitcnt vmcnt(2)
	v_mov_b32_e32 v92, v64
	v_mov_b64_e32 v[88:89], v[34:35]
	v_mov_b64_e32 v[76:77], v[38:39]
	global_store_dwordx2 v[62:63], v[60:61], off
	v_mov_b64_e32 v[68:69], v[42:43]
	v_mov_b64_e32 v[84:85], v[46:47]
	v_mov_b64_e32 v[80:81], v[50:51]
	v_mov_b64_e32 v[72:73], v[54:55]
	v_mov_b64_e32 v[62:63], v[58:59]
	v_mov_b64_e32 v[86:87], v[32:33]
	v_mov_b64_e32 v[74:75], v[36:37]
	v_mov_b64_e32 v[66:67], v[40:41]
	v_mov_b64_e32 v[82:83], v[44:45]
	v_mov_b64_e32 v[78:79], v[48:49]
	v_mov_b64_e32 v[70:71], v[52:53]
	v_mov_b64_e32 v[60:61], v[56:57]
	s_cbranch_scc0 .LBB0_1651

.LBB0_1918:
	s_and_saveexec_b64 s[4:5], s[48:49]
	ds_write_b32 v79, v65
	s_or_b64 exec, exec, s[4:5]
	v_cndmask_b32_e64 v52, 0, 1, s[62:63]
	v_cmp_ne_u32_e64 s[52:53], 1, v52
	s_andn2_b64 vcc, exec, s[62:63]
	s_lshl_b32 s13, s12, 6
	s_waitcnt lgkmcnt(0)
	s_barrier
	s_cbranch_vccnz .LBB0_1923
	s_add_i32 s4, s13, s82
	s_ashr_i32 s5, s4, 31
	s_lshl_b64 s[4:5], s[4:5], 11
	v_lshl_add_u64 v[56:57], v[32:33], 0, s[4:5]
	global_load_dwordx2 v[52:53], v[56:57], off offset:1536
	global_load_dwordx2 v[54:55], v[56:57], off offset:1024
	global_load_dwordx2 v[60:61], v[56:57], off offset:512
	global_load_dwordx2 v[62:63], v[56:57], off
	s_mov_b32 s15, s82
	s_waitcnt vmcnt(0)
.LBB0_1922:
	s_waitcnt vmcnt(8)
	v_lshlrev_b32_e32 v71, 16, v63
	v_lshlrev_b32_e32 v70, 16, v62
	v_and_b32_e32 v63, 0xffff0000, v63
	v_and_b32_e32 v62, 0xffff0000, v62
	v_pk_add_f32 v[72:73], v[70:71], v[62:63]
	v_lshlrev_b32_e32 v66, 16, v54
	v_add_f32_e32 v64, v72, v73
	v_lshlrev_b32_e32 v73, 16, v61
	v_lshlrev_b32_e32 v72, 16, v60
	v_and_b32_e32 v61, 0xffff0000, v61
	v_and_b32_e32 v60, 0xffff0000, v60
	v_pk_add_f32 v[74:75], v[72:73], v[60:61]
	v_and_b32_e32 v67, 0xffff0000, v54
	v_lshlrev_b32_e32 v68, 16, v55
	v_and_b32_e32 v69, 0xffff0000, v55
	v_pk_add_f32 v[74:75], v[74:75], v[74:75] op_sel_hi:[0,1]
	v_lshlrev_b32_e32 v94, 16, v52
	v_and_b32_e32 v96, 0xffff0000, v52
	v_lshlrev_b32_e32 v98, 16, v53
	v_and_b32_e32 v100, 0xffff0000, v53
	v_add_f32_e32 v101, 0, v64
	v_add_f32_e32 v95, v66, v67
	v_add_f32_e32 v97, v68, v69
	v_mov_b32_e32 v99, v75
	v_pk_add_f32 v[76:77], v[94:95], v[96:97]
	v_pk_add_f32 v[74:75], v[98:99], v[100:101]
	s_add_i32 s14, s15, 8
	v_pk_add_f32 v[74:75], v[76:77], v[74:75]
	s_cmp_lt_i32 s15, 56
	v_add_f32_e32 v64, v74, v75
	s_cselect_b32 s4, s14, s15
	s_add_i32 s4, s4, s13
	v_add_f32_dpp v64, v64, v64 quad_perm:[1,0,3,2] row_mask:0xf bank_mask:0xf bound_ctrl:1
	s_ashr_i32 s5, s4, 31
	s_lshl_b64 s[16:17], s[4:5], 11
	v_add_f32_dpp v64, v64, v64 quad_perm:[2,3,0,1] row_mask:0xf bank_mask:0xf bound_ctrl:1
	v_lshl_add_u64 v[52:53], v[32:33], 0, s[16:17]
	global_load_dwordx2 v[56:57], v[52:53], off
	global_load_dwordx2 v[58:59], v[52:53], off offset:512
	global_load_dwordx2 v[54:55], v[52:53], off offset:1024
	s_nop 0
	global_load_dwordx2 v[52:53], v[52:53], off offset:1536
	v_add_f32_dpp v64, v64, v64 row_ror:4 row_mask:0xf bank_mask:0xf bound_ctrl:1
	s_add_i32 s6, s9, s15
	s_ashr_i32 s7, s6, 31
	v_add_f32_dpp v64, v64, v64 row_ror:8 row_mask:0xf bank_mask:0xf bound_ctrl:1
	ds_swizzle_b32 v74, v64 offset:swizzle(SWAP,16)
	s_lshl_b64 s[4:5], s[6:7], 10
	s_lshl_b64 s[6:7], s[6:7], 11
	s_cmp_gt_i32 s15, 55
	s_mov_b32 s15, s14
	s_waitcnt lgkmcnt(0)
	v_add_f32_e32 v64, v64, v74
	v_mbcnt_lo_u32_b32 v74, -1, 0
	v_mbcnt_hi_u32_b32 v74, -1, v74
	s_nop 0
	v_lshlrev_b32_e32 v74, 2, v74
	v_xor_b32_e32 v74, 0x80, v74
	ds_bpermute_b32 v74, v74, v64
	s_waitcnt lgkmcnt(0)
	v_add_f32_e32 v64, v64, v74
	v_fmac_f32_e32 v62, 0xba800000, v64
	v_fmac_f32_e32 v63, 0xba800000, v64
	v_fmac_f32_e32 v71, 0xba800000, v64
	v_fmac_f32_e32 v70, 0xba800000, v64
	v_mov_b32_e32 v74, v71
	v_mov_b32_e32 v75, v63
	v_mov_b32_e32 v71, v62
	v_pk_mul_f32 v[76:77], v[74:75], v[74:75]
	v_pk_mul_f32 v[62:63], v[70:71], v[70:71]
	v_fmac_f32_e32 v60, 0xba800000, v64
	v_pk_mov_b32 v[102:103], v[62:63], v[76:77] op_sel:[1,0]
	v_mov_b32_e32 v63, v77
	v_fmac_f32_e32 v61, 0xba800000, v64
	v_fmac_f32_e32 v73, 0xba800000, v64
	v_pk_add_f32 v[62:63], v[102:103], v[62:63]
	v_fmac_f32_e32 v72, 0xba800000, v64
	v_mov_b32_e32 v102, v73
	v_mov_b32_e32 v103, v61
	v_mov_b32_e32 v73, v60
	v_pk_mul_f32 v[76:77], v[102:103], v[102:103]
	v_pk_mul_f32 v[60:61], v[72:73], v[72:73]
	v_fmac_f32_e32 v66, 0xba800000, v64
	v_pk_mov_b32 v[104:105], v[60:61], v[76:77] op_sel:[1,0]
	v_mov_b32_e32 v61, v77
	v_pk_add_f32 v[60:61], v[104:105], v[60:61]
	v_fmac_f32_e32 v67, 0xba800000, v64
	v_pk_add_f32 v[60:61], v[60:61], v[60:61] op_sel_hi:[0,1]
	v_fmac_f32_e32 v68, 0xba800000, v64
	v_mul_f32_e32 v60, v66, v66
	v_fmac_f32_e32 v69, 0xba800000, v64
	v_pk_fma_f32 v[76:77], v[66:67], v[66:67], v[60:61] op_sel_hi:[1,1,0]
	v_mul_f32_e32 v60, v68, v68
	v_pk_add_f32 v[62:63], v[62:63], v[62:63] op_sel_hi:[0,1]
	v_pk_fma_f32 v[104:105], v[68:69], v[68:69], v[60:61] op_sel_hi:[1,1,0]
	v_fmac_f32_e32 v100, 0xba800000, v64
	v_fmac_f32_e32 v98, 0xba800000, v64
	v_fmac_f32_e32 v96, 0xba800000, v64
	v_fmac_f32_e32 v94, 0xba800000, v64
	v_mul_f32_e32 v76, v94, v94
	v_mul_f32_e32 v104, v96, v96
	v_mul_f32_e32 v62, v98, v98
	v_mul_f32_e32 v60, v100, v100
	v_pk_add_f32 v[76:77], v[76:77], v[104:105]
	v_pk_add_f32 v[60:61], v[62:63], v[60:61]
	v_mov_b32_e32 v95, v96
	v_pk_add_f32 v[60:61], v[76:77], v[60:61]
	v_mov_b32_e32 v99, v100
	v_add_f32_e32 v60, v60, v61
	s_nop 1
	v_add_f32_dpp v60, v60, v60 quad_perm:[1,0,3,2] row_mask:0xf bank_mask:0xf bound_ctrl:1
	s_nop 1
	v_add_f32_dpp v60, v60, v60 quad_perm:[2,3,0,1] row_mask:0xf bank_mask:0xf bound_ctrl:1
	s_nop 1
	v_add_f32_dpp v60, v60, v60 row_ror:4 row_mask:0xf bank_mask:0xf bound_ctrl:1
	s_nop 1
	v_add_f32_dpp v60, v60, v60 row_ror:8 row_mask:0xf bank_mask:0xf bound_ctrl:1
	ds_swizzle_b32 v61, v60 offset:swizzle(SWAP,16)
	s_waitcnt lgkmcnt(0)
	v_add_f32_e32 v60, v60, v61
	v_mbcnt_lo_u32_b32 v61, -1, 0
	v_mbcnt_hi_u32_b32 v61, -1, v61
	s_nop 0
	v_lshlrev_b32_e32 v61, 2, v61
	v_xor_b32_e32 v61, 0x80, v61
	ds_bpermute_b32 v61, v61, v60
	s_waitcnt lgkmcnt(0)
	v_add_f32_e32 v60, v60, v61
	v_fmamk_f32 v60, v60, 0x3a800000, v218
	v_cmp_gt_f32_e32 vcc, s28, v60
	v_mul_f32_e32 v61, 0x4b800000, v60
	s_nop 0
	v_cndmask_b32_e32 v60, v60, v61, vcc
	v_rsq_f32_e32 v60, v60
	s_nop 0
	v_mul_f32_e32 v61, 0x45800000, v60
	v_cndmask_b32_e32 v60, v60, v61, vcc
	v_pk_mul_f32 v[62:63], v[70:71], v[60:61] op_sel_hi:[1,0]
	v_pk_mul_f32 v[70:71], v[74:75], v[60:61] op_sel_hi:[1,0]
	v_pk_fma_f32 v[104:105], v[0:1], v[62:63], v[8:9]
	v_pk_fma_f32 v[76:77], v[2:3], v[70:71], v[10:11]
	v_pk_mul_f32 v[62:63], v[72:73], v[60:61] op_sel_hi:[1,0]
	v_pk_mul_f32 v[70:71], v[102:103], v[60:61] op_sel_hi:[1,0]
	v_pk_mul_f32 v[66:67], v[66:67], v[60:61] op_sel_hi:[1,0]
	v_pk_fma_f32 v[72:73], v[6:7], v[70:71], v[14:15]
	v_pk_fma_f32 v[74:75], v[4:5], v[62:63], v[12:13]
	v_pk_mul_f32 v[62:63], v[68:69], v[60:61] op_sel_hi:[1,0]
	v_pk_fma_f32 v[70:71], v[16:17], v[66:67], v[24:25]
	v_pk_mul_f32 v[66:67], v[94:95], v[60:61] op_sel_hi:[1,0]
	v_lshl_add_u64 v[68:69], v[34:35], 0, s[6:7]
	v_cvt_pk_bf16_f32 v94, v104, v105
	v_cvt_pk_bf16_f32 v95, v76, v77
	global_store_dwordx2 v[68:69], v[94:95], off
	v_mul_f32_e32 v64, 0x41800000, v104
	v_mul_f32_e32 v94, 0x41800000, v105
	v_mov_b32_e32 v95, v65
	v_cvt_pk_fp8_f32 v95, v64, v94
	v_mul_f32_e32 v64, 0x41800000, v76
	v_mul_f32_e32 v76, 0x41800000, v77
	v_pk_fma_f32 v[62:63], v[18:19], v[62:63], v[26:27]
	v_cvt_pk_fp8_f32 v95, v64, v76 op_sel:[0,0,1]
	v_lshl_add_u64 v[76:77], v[40:41], 0, s[4:5]
	v_mul_f32_e32 v64, 0x41800000, v74
	v_pk_mul_f32 v[60:61], v[98:99], v[60:61] op_sel_hi:[1,0]
	global_store_dword v[76:77], v95, off
	v_cvt_pk_bf16_f32 v76, v74, v75
	v_mul_f32_e32 v74, 0x41800000, v75
	v_mov_b32_e32 v75, v65
	v_cvt_pk_fp8_f32 v75, v64, v74
	v_cvt_pk_bf16_f32 v77, v72, v73
	v_mul_f32_e32 v64, 0x41800000, v72
	v_mul_f32_e32 v72, 0x41800000, v73
	v_cvt_pk_fp8_f32 v75, v64, v72 op_sel:[0,0,1]
	v_cvt_pk_bf16_f32 v74, v70, v71
	v_mul_f32_e32 v64, 0x41800000, v70
	v_mul_f32_e32 v70, 0x41800000, v71
	v_mov_b32_e32 v71, v65
	v_lshl_add_u64 v[72:73], v[38:39], 0, s[4:5]
	s_mov_b32 s4, 0x8d600000
	v_cvt_pk_fp8_f32 v71, v64, v70
	v_add_co_u32_e32 v72, vcc, s4, v72
	global_store_dwordx2 v[68:69], v[76:77], off offset:512
	s_nop 0
	v_addc_co_u32_e32 v73, vcc, 0, v73, vcc
	global_store_dword v[72:73], v75, off offset:256
	v_cvt_pk_bf16_f32 v75, v62, v63
	v_mul_f32_e32 v62, 0x41800000, v62
	v_mul_f32_e32 v63, 0x41800000, v63
	v_cvt_pk_fp8_f32 v71, v62, v63 op_sel:[0,0,1]
	v_pk_fma_f32 v[60:61], v[22:23], v[60:61], v[30:31]
	v_pk_fma_f32 v[66:67], v[20:21], v[66:67], v[28:29]
	v_cvt_pk_bf16_f32 v63, v60, v61
	v_cvt_pk_bf16_f32 v62, v66, v67
	global_store_dwordx2 v[68:69], v[74:75], off offset:1024
	global_store_dword v[72:73], v71, off offset:512
	global_store_dwordx2 v[68:69], v[62:63], off offset:1536
	v_mul_f32_e32 v62, 0x41800000, v66
	v_mul_f32_e32 v63, 0x41800000, v67
	v_mov_b32_e32 v64, v65
	v_cvt_pk_fp8_f32 v64, v62, v63
	v_mul_f32_e32 v60, 0x41800000, v60
	v_mul_f32_e32 v61, 0x41800000, v61
	s_waitcnt vmcnt(10)
	v_mov_b64_e32 v[62:63], v[56:57]
	v_cvt_pk_fp8_f32 v64, v60, v61 op_sel:[0,0,1]
	s_waitcnt vmcnt(9)
	v_mov_b64_e32 v[60:61], v[58:59]
	global_store_dword v[72:73], v64, off offset:768
	s_cbranch_scc0 .LBB0_1922

.LBB0_2248:
	s_ashr_i32 s6, s5, 2
	s_add_i32 s6, s6, s13
	s_ashr_i32 s7, s6, 31
	s_lshl_b64 s[6:7], s[6:7], 11
	v_lshl_add_u64 v[56:57], v[48:49], 0, s[6:7]
	global_load_dwordx4 v[120:123], v[56:57], off
	global_load_dwordx4 v[124:127], v[56:57], off offset:1024
	s_waitcnt vmcnt(0)
.Lrc_loop:
	v_mov_b32_e32 v62, s4
	s_addk_i32 s4, 0x180
	s_cmpk_gt_i32 s5, 0xdf
	s_cselect_b32 s22, 1, 0
	s_add_i32 s5, s5, 32
	s_waitcnt vmcnt(8)
	v_lshlrev_b32_e32 v60, 16, v120
	v_and_b32_e32 v61, 0xffff0000, v120
	v_mul_f32_e32 v60, 0x41800000, v60
	v_mul_f32_e32 v61, 0x41800000, v61
	v_mov_b32_e32 v52, v65
	s_nop 0
	v_cvt_pk_fp8_f32 v52, v60, v61
	v_lshlrev_b32_e32 v60, 16, v121
	v_and_b32_e32 v61, 0xffff0000, v121
	v_mul_f32_e32 v60, 0x41800000, v60
	v_mul_f32_e32 v61, 0x41800000, v61
	v_cvt_pk_fp8_f32 v52, v60, v61 op_sel:[0,0,1]
	v_lshlrev_b32_e32 v60, 16, v122
	v_and_b32_e32 v61, 0xffff0000, v122
	v_mul_f32_e32 v60, 0x41800000, v60
	v_mul_f32_e32 v61, 0x41800000, v61
	v_mov_b32_e32 v53, v65
	s_nop 0
	v_cvt_pk_fp8_f32 v53, v60, v61
	v_lshlrev_b32_e32 v60, 16, v123
	v_and_b32_e32 v61, 0xffff0000, v123
	v_mul_f32_e32 v60, 0x41800000, v60
	v_mul_f32_e32 v61, 0x41800000, v61
	v_cvt_pk_fp8_f32 v53, v60, v61 op_sel:[0,0,1]
	v_lshlrev_b32_e32 v60, 16, v124
	v_and_b32_e32 v61, 0xffff0000, v124
	v_mul_f32_e32 v60, 0x41800000, v60
	v_mul_f32_e32 v61, 0x41800000, v61
	v_mov_b32_e32 v54, v65
	s_nop 0
	v_cvt_pk_fp8_f32 v54, v60, v61
	v_lshlrev_b32_e32 v60, 16, v125
	v_and_b32_e32 v61, 0xffff0000, v125
	v_mul_f32_e32 v60, 0x41800000, v60
	v_mul_f32_e32 v61, 0x41800000, v61
	v_cvt_pk_fp8_f32 v54, v60, v61 op_sel:[0,0,1]
	v_lshlrev_b32_e32 v60, 16, v126
	v_and_b32_e32 v61, 0xffff0000, v126
	v_mul_f32_e32 v60, 0x41800000, v60
	v_mul_f32_e32 v61, 0x41800000, v61
	v_mov_b32_e32 v55, v65
	s_nop 0
	v_cvt_pk_fp8_f32 v55, v60, v61
	v_lshlrev_b32_e32 v60, 16, v127
	v_and_b32_e32 v61, 0xffff0000, v127
	v_mul_f32_e32 v60, 0x41800000, v60
	v_mul_f32_e32 v61, 0x41800000, v61
	v_cvt_pk_fp8_f32 v55, v60, v61 op_sel:[0,0,1]
	s_cmp_eq_u32 s22, 1
	s_cbranch_scc1 .Lrc_nold
	s_ashr_i32 s6, s5, 2
	s_add_i32 s6, s6, s13
	s_ashr_i32 s7, s6, 31
	s_lshl_b64 s[6:7], s[6:7], 11
	v_lshl_add_u64 v[56:57], v[48:49], 0, s[6:7]
	global_load_dwordx4 v[120:123], v[56:57], off
	global_load_dwordx4 v[124:127], v[56:57], off offset:1024
.Lrc_nold:
	ds_read2_b64 v[56:59], v62 offset1:3
	s_waitcnt lgkmcnt(0)
	v_mov_b32_e32 v64, v56
	v_lshlrev_b32_e32 v56, 2, v56
	v_add_u32_e32 v56, s2, v56
	ds_read_b32 v56, v56
	v_lshlrev_b64 v[60:61], 24, v[64:65]
	v_lshl_add_u64 v[60:61], s[58:59], 0, v[60:61]
	s_waitcnt lgkmcnt(0)
	v_add_u32_e32 v56, v56, v57
	v_mov_b32_e32 v57, v65
	v_lshlrev_b64 v[56:57], 10, v[56:57]
	v_lshl_add_u64 v[56:57], v[60:61], 0, v[56:57]
	v_lshl_add_u64 v[56:57], v[56:57], 0, v[50:51]
	global_store_dwordx2 v[56:57], v[52:53], off
	global_store_dwordx2 v[56:57], v[54:55], off offset:512
	ds_read2_b32 v[56:57], v62 offset0:3 offset1:4
	s_waitcnt lgkmcnt(0)
	v_mov_b32_e32 v64, v56
	v_lshlrev_b32_e32 v56, 2, v56
	v_add_u32_e32 v56, s2, v56
	ds_read_b32 v56, v56
	v_lshlrev_b64 v[60:61], 24, v[64:65]
	v_lshl_add_u64 v[60:61], s[58:59], 0, v[60:61]
	v_mov_b32_e32 v64, v58
	s_waitcnt lgkmcnt(0)
	v_add_u32_e32 v56, v56, v57
	v_mov_b32_e32 v57, v65
	v_lshlrev_b64 v[56:57], 10, v[56:57]
	v_lshl_add_u64 v[56:57], v[60:61], 0, v[56:57]
	v_lshl_add_u64 v[56:57], v[56:57], 0, v[50:51]
	global_store_dwordx2 v[56:57], v[52:53], off
	global_store_dwordx2 v[56:57], v[54:55], off offset:512
	v_lshlrev_b32_e32 v56, 2, v58
	v_add_u32_e32 v56, s2, v56
	ds_read_b32 v56, v56
	v_mov_b32_e32 v57, v65
	s_waitcnt lgkmcnt(0)
	v_add_u32_e32 v56, v56, v59
	v_lshlrev_b64 v[58:59], 24, v[64:65]
	v_lshlrev_b64 v[56:57], 10, v[56:57]
	v_lshl_add_u64 v[58:59], s[58:59], 0, v[58:59]
	v_lshl_add_u64 v[56:57], v[58:59], 0, v[56:57]
	v_lshl_add_u64 v[56:57], v[56:57], 0, v[50:51]
	global_store_dwordx2 v[56:57], v[52:53], off
	global_store_dwordx2 v[56:57], v[54:55], off offset:512
	ds_read2_b32 v[56:57], v62 offset0:9 offset1:10
	s_waitcnt lgkmcnt(0)
	v_mov_b32_e32 v64, v56
	v_lshlrev_b32_e32 v56, 2, v56
	v_add_u32_e32 v56, s2, v56
	ds_read_b32 v56, v56
	v_lshlrev_b64 v[58:59], 24, v[64:65]
	v_lshl_add_u64 v[58:59], s[58:59], 0, v[58:59]
	s_waitcnt lgkmcnt(0)
	v_add_u32_e32 v56, v56, v57
	v_mov_b32_e32 v57, v65
	v_lshlrev_b64 v[56:57], 10, v[56:57]
	v_lshl_add_u64 v[56:57], v[58:59], 0, v[56:57]
	v_lshl_add_u64 v[56:57], v[56:57], 0, v[50:51]
	global_store_dwordx2 v[56:57], v[52:53], off
	global_store_dwordx2 v[56:57], v[54:55], off offset:512
	s_cmp_eq_u32 s22, 1
	s_cbranch_scc0 .Lrc_loop
	s_branch .LBB0_1917

.LBB0_2492:
	s_lshl_b32 s20, s91, 3
	s_abs_i32 s7, s20
	v_cvt_f32_u32_e32 v1, s7
	s_lshl_b32 s6, s93, 3
	s_add_i32 s6, s6, s82
	s_sub_i32 s8, s20, s6
	v_rcp_iflag_f32_e32 v1, v1
	s_add_i32 s12, s8, 0x3fff
	s_sub_i32 s8, 0xffffc001, s8
	s_xor_b32 s13, s12, s20
	v_mul_f32_e32 v1, 0x4f7ffffe, v1
	v_cvt_u32_f32_e32 v1, v1
	s_sub_i32 s9, 0, s7
	s_max_i32 s8, s12, s8
	s_ashr_i32 s12, s13, 31
	v_readfirstlane_b32 s13, v1
	s_mul_i32 s9, s9, s13
	s_mul_hi_u32 s9, s13, s9
	s_add_i32 s13, s13, s9
	s_mul_hi_u32 s9, s8, s13
	s_mul_i32 s13, s9, s7
	s_sub_i32 s8, s8, s13
	s_add_i32 s13, s9, 1
	s_sub_i32 s14, s8, s7
	s_cmp_ge_u32 s8, s7
	s_cselect_b32 s9, s13, s9
	s_cselect_b32 s8, s14, s8
	s_add_i32 s13, s9, 1
	s_cmp_ge_u32 s8, s7
	s_cselect_b32 s7, s13, s9
	s_xor_b32 s7, s7, s12
	s_sub_i32 s21, s7, s12
	s_cmp_lt_i32 s21, 1
	s_cbranch_scc1 .LBB0_2501
	s_waitcnt lgkmcnt(0)
	s_add_u32 s14, s10, 0x8a200000
	s_addc_u32 s15, s11, 0
	s_add_u32 s22, s10, 0x8c500000
	s_load_dwordx4 s[24:27], s[4:5], 0x158
	s_addc_u32 s23, s11, 0
	s_add_u32 s16, s10, 0xa7600000
	v_readlane_b32 s38, v255, 4
	s_addc_u32 s17, s11, 0
	s_lshl_b32 s34, s38, 10
	s_lshl_b64 s[8:9], s[34:35], 2
	s_waitcnt lgkmcnt(0)
	s_add_u32 s12, s24, s8
	s_addc_u32 s13, s25, s9
	s_add_u32 s8, s26, s8
	s_addc_u32 s9, s27, s9
	v_lshlrev_b32_e32 v52, 2, v0
	v_ashrrev_i32_e32 v53, 31, v52
	s_add_u32 s24, s10, 0x8c400000
	v_lshlrev_b64 v[0:1], 2, v[52:53]
	s_addc_u32 s25, s11, 0
	v_lshl_add_u64 v[28:29], s[8:9], 0, v[0:1]
	s_add_u32 s8, s10, 0x9e600000
	v_lshlrev_b64 v[32:33], 1, v[52:53]
	v_lshl_add_u64 v[24:25], s[12:13], 0, v[0:1]
	s_addc_u32 s9, s11, 0
	v_lshl_add_u64 v[34:35], s[10:11], 0, v[32:33]
	s_mov_b64 s[12:13], 0x42000000
	s_ashr_i32 s7, s6, 31
	v_lshl_add_u64 v[58:59], v[34:35], 0, s[12:13]
	s_lshl_b64 s[12:13], s[6:7], 4
	s_add_u32 s18, s24, s12
	s_addc_u32 s19, s25, s13
	global_load_dwordx4 v[0:3], v[24:25], off
	global_load_dwordx4 v[4:7], v[28:29], off
	global_load_dwordx4 v[8:11], v[24:25], off offset:1024
	global_load_dwordx4 v[12:15], v[28:29], off offset:1024
	global_load_dwordx4 v[16:19], v[24:25], off offset:2048
	global_load_dwordx4 v[20:23], v[28:29], off offset:2048
	s_nop 0
	global_load_dwordx4 v[24:27], v[24:25], off offset:3072
	s_nop 0
	global_load_dwordx4 v[28:31], v[28:29], off offset:3072
	v_lshl_add_u64 v[56:57], s[16:17], 0, v[32:33]
	global_load_dwordx4 v[34:37], v65, s[18:19]
	v_lshl_add_u64 v[54:55], s[14:15], 0, v[32:33]
	v_lshl_add_u64 v[60:61], s[10:11], 0, v[52:53]
	s_mov_b64 s[10:11], 0x8c600000
	v_lshl_add_u64 v[62:63], v[60:61], 0, s[10:11]
	v_readlane_b32 s39, v255, 5
	s_waitcnt vmcnt(0)
	v_readfirstlane_b32 s33, v37
	s_lshr_b32 s26, s33, 18
	s_and_b32 s34, s26, 0x3ffc
	s_add_i32 s26, 0, 0x20000
	s_add_i32 s34, s26, s34
	v_readfirstlane_b32 s18, v34
	v_mov_b32_e32 v34, s34
	ds_read_b32 v64, v34 offset:1408
	v_readfirstlane_b32 s19, v35
	v_readfirstlane_b32 s27, v36
	s_lshl_b32 s33, s33, 10
	s_and_b32 s34, s33, 0x3ffffc00
	s_waitcnt lgkmcnt(0)
	v_lshlrev_b64 v[34:35], 18, v[64:65]
	v_lshl_add_u64 v[34:35], s[8:9], 0, v[34:35]
	s_lshr_b32 s33, s27, 18
	v_lshl_add_u64 v[34:35], v[34:35], 0, s[34:35]
	s_and_b32 s33, s33, 0x3ffc
	v_lshl_add_u64 v[34:35], v[34:35], 0, v[52:53]
	s_add_i32 s33, s26, s33
	global_load_dword v94, v[34:35], off offset:768 nt
	global_load_dword v95, v[34:35], off offset:512 nt
	global_load_dword v96, v[34:35], off offset:256 nt
	global_load_dword v97, v[34:35], off nt
	v_mov_b32_e32 v34, s33
	ds_read_b32 v64, v34 offset:1408
	s_lshl_b32 s27, s27, 10
	s_and_b32 s34, s27, 0x3ffffc00
	s_lshr_b32 s27, s19, 18
	s_and_b32 s27, s27, 0x3ffc
	s_waitcnt lgkmcnt(0)
	v_lshlrev_b64 v[34:35], 18, v[64:65]
	v_lshl_add_u64 v[34:35], s[8:9], 0, v[34:35]
	v_lshl_add_u64 v[34:35], v[34:35], 0, s[34:35]
	v_lshl_add_u64 v[34:35], v[34:35], 0, v[52:53]
	s_add_i32 s27, s26, s27
	global_load_dword v98, v[34:35], off offset:768 nt
	global_load_dword v99, v[34:35], off offset:512 nt
	global_load_dword v100, v[34:35], off offset:256 nt
	global_load_dword v101, v[34:35], off nt
	v_mov_b32_e32 v34, s27
	ds_read_b32 v64, v34 offset:1408
	s_lshl_b32 s19, s19, 10
	s_and_b32 s34, s19, 0x3ffffc00
	s_lshr_b32 s19, s18, 18
	s_and_b32 s19, s19, 0x3ffc
	s_waitcnt lgkmcnt(0)
	v_lshlrev_b64 v[34:35], 18, v[64:65]
	v_lshl_add_u64 v[34:35], s[8:9], 0, v[34:35]
	v_lshl_add_u64 v[34:35], v[34:35], 0, s[34:35]
	v_lshl_add_u64 v[34:35], v[34:35], 0, v[52:53]
	s_add_i32 s19, s26, s19
	global_load_dword v102, v[34:35], off offset:768 nt
	global_load_dword v103, v[34:35], off offset:512 nt
	global_load_dword v104, v[34:35], off offset:256 nt
	global_load_dword v105, v[34:35], off nt
	v_mov_b32_e32 v34, s19
	ds_read_b32 v64, v34 offset:1408
	s_lshl_b32 s18, s18, 10
	s_and_b32 s34, s18, 0x3ffffc00
	s_lshl_b64 s[18:19], s[6:7], 11
	s_add_u32 s16, s16, s18
	s_waitcnt lgkmcnt(0)
	v_lshlrev_b64 v[34:35], 18, v[64:65]
	s_addc_u32 s17, s17, s19
	v_lshl_add_u64 v[34:35], s[8:9], 0, v[34:35]
	s_add_u32 s14, s14, s18
	v_lshl_add_u64 v[34:35], v[34:35], 0, s[34:35]
	s_addc_u32 s15, s15, s19
	v_lshl_add_u64 v[34:35], v[34:35], 0, v[52:53]
	s_cmp_lg_u32 s21, 1
	global_load_dword v106, v[34:35], off offset:768 nt
	global_load_dword v107, v[34:35], off offset:512 nt
	global_load_dword v108, v[34:35], off offset:256 nt
	global_load_dword v109, v[34:35], off nt
	v_lshl_add_u64 v[34:35], s[16:17], 0, v[32:33]
	v_lshl_add_u64 v[32:33], s[14:15], 0, v[32:33]
	s_cselect_b32 s14, s20, 0
	s_add_i32 s14, s14, s6
	s_ashr_i32 s15, s14, 31
	s_lshl_b64 s[14:15], s[14:15], 4
	s_add_u32 s16, s22, s14
	s_addc_u32 s17, s23, s15
	s_add_u32 s14, s24, s14
	s_addc_u32 s15, s25, s15
	global_load_dwordx2 v[44:45], v[34:35], off offset:1536 nt
	global_load_dwordx2 v[46:47], v[32:33], off offset:1536 nt
	global_load_dwordx2 v[48:49], v[34:35], off offset:1024 nt
	global_load_dwordx2 v[50:51], v[32:33], off offset:1024 nt
	global_load_dwordx2 v[86:87], v[34:35], off offset:512 nt
	global_load_dwordx2 v[88:89], v[32:33], off offset:512 nt
	global_load_dwordx2 v[90:91], v[34:35], off nt
	global_load_dwordx2 v[92:93], v[32:33], off nt
	global_load_dwordx4 v[36:39], v65, s[14:15]
	s_add_u32 s12, s22, s12
	global_load_dwordx4 v[32:35], v65, s[16:17]
	s_addc_u32 s13, s23, s13
	s_cmp_lg_u32 s38, 3
	s_mov_b32 s7, 0
	s_waitcnt vmcnt(1)
	v_readfirstlane_b32 s16, v39
	v_readfirstlane_b32 s17, v38
	v_readfirstlane_b32 s18, v37
	v_readfirstlane_b32 s19, v36
	global_load_dwordx4 v[36:39], v65, s[12:13]
	s_cselect_b64 s[12:13], -1, 0
	s_lshl_b32 s14, s91, 4
	s_waitcnt vmcnt(0)
	s_branch .LBB0_2495
.Lcomb_skip:
	s_waitcnt vmcnt(0)
	s_branch .LBB0_2497

.LBB0_2495:
	s_add_i32 s15, s7, 1
	s_cmp_ge_i32 s15, s21
	s_cbranch_scc1 .Lcomb_skip
	s_add_i32 s10, s20, s6
	s_ashr_i32 s11, s10, 31
	s_lshl_b64 s[10:11], s[10:11], 11
	v_lshl_add_u64 v[40:41], v[54:55], 0, s[10:11]
	v_lshl_add_u64 v[42:43], v[56:57], 0, s[10:11]
	s_lshr_b32 s10, s19, 18
	s_and_b32 s10, s10, 0x3ffc
	s_add_i32 s10, s26, s10
	global_load_dwordx2 v[66:67], v[40:41], off nt
	global_load_dwordx2 v[68:69], v[40:41], off offset:512 nt
	global_load_dwordx2 v[70:71], v[40:41], off offset:1024 nt
	global_load_dwordx2 v[72:73], v[40:41], off offset:1536 nt
	v_mov_b32_e32 v40, s10
	ds_read_b32 v64, v40 offset:1408
	s_lshl_b32 s10, s19, 10
	s_and_b32 s34, s10, 0x3ffffc00
	s_lshr_b32 s10, s18, 18
	s_and_b32 s10, s10, 0x3ffc
	s_add_i32 s10, s26, s10
	global_load_dwordx2 v[74:75], v[42:43], off nt
	global_load_dwordx2 v[76:77], v[42:43], off offset:512 nt
	global_load_dwordx2 v[78:79], v[42:43], off offset:1024 nt
	global_load_dwordx2 v[80:81], v[42:43], off offset:1536 nt
	v_mov_b32_e32 v42, s10
	s_waitcnt lgkmcnt(0)
	v_lshlrev_b64 v[40:41], 18, v[64:65]
	ds_read_b32 v64, v42 offset:1408
	v_lshl_add_u64 v[40:41], s[8:9], 0, v[40:41]
	s_lshl_b32 s10, s18, 10
	v_lshl_add_u64 v[40:41], v[40:41], 0, s[34:35]
	s_and_b32 s34, s10, 0x3ffffc00
	s_lshr_b32 s10, s17, 18
	s_and_b32 s10, s10, 0x3ffc
	v_lshl_add_u64 v[40:41], v[40:41], 0, v[52:53]
	s_add_i32 s10, s26, s10
	global_load_dword v110, v[40:41], off nt
	global_load_dword v111, v[40:41], off offset:256 nt
	global_load_dword v112, v[40:41], off offset:512 nt
	global_load_dword v113, v[40:41], off offset:768 nt
	s_waitcnt lgkmcnt(0)
	v_lshlrev_b64 v[40:41], 18, v[64:65]
	v_mov_b32_e32 v42, s10
	v_lshl_add_u64 v[40:41], s[8:9], 0, v[40:41]
	ds_read_b32 v64, v42 offset:1408
	s_lshl_b32 s10, s17, 10
	v_lshl_add_u64 v[40:41], v[40:41], 0, s[34:35]
	s_and_b32 s34, s10, 0x3ffffc00
	s_lshr_b32 s10, s16, 18
	s_and_b32 s10, s10, 0x3ffc
	s_add_i32 s10, s26, s10
	v_lshl_add_u64 v[40:41], v[40:41], 0, v[52:53]
	v_mov_b32_e32 v42, s10
	global_load_dword v114, v[40:41], off nt
	global_load_dword v115, v[40:41], off offset:256 nt
	global_load_dword v116, v[40:41], off offset:512 nt
	global_load_dword v117, v[40:41], off offset:768 nt
	s_waitcnt lgkmcnt(0)
	v_lshlrev_b64 v[40:41], 18, v[64:65]
	ds_read_b32 v64, v42 offset:1408
	v_lshl_add_u64 v[40:41], s[8:9], 0, v[40:41]
	v_lshl_add_u64 v[40:41], v[40:41], 0, s[34:35]
	v_lshl_add_u64 v[40:41], v[40:41], 0, v[52:53]
	global_load_dword v118, v[40:41], off nt
	global_load_dword v119, v[40:41], off offset:256 nt
	global_load_dword v120, v[40:41], off offset:512 nt
	global_load_dword v121, v[40:41], off offset:768 nt
	s_waitcnt lgkmcnt(0)
	v_lshlrev_b64 v[40:41], 18, v[64:65]
	s_lshl_b32 s10, s16, 10
	s_and_b32 s34, s10, 0x3ffffc00
	v_lshl_add_u64 v[40:41], s[8:9], 0, v[40:41]
	v_lshl_add_u64 v[40:41], v[40:41], 0, s[34:35]
	v_lshl_add_u64 v[40:41], v[40:41], 0, v[52:53]
	global_load_dword v64, v[40:41], off nt
	global_load_dword v122, v[40:41], off offset:256 nt
	global_load_dword v123, v[40:41], off offset:512 nt
	global_load_dword v124, v[40:41], off offset:768 nt
	s_waitcnt vmcnt(28)
	v_mov_b64_e32 v[82:83], v[34:35]
	v_mov_b64_e32 v[84:85], v[32:33]
.LBB0_2497:
	s_add_i32 s7, s7, 2
	s_cmp_lt_i32 s7, s21
	s_cselect_b32 s7, s14, 0
	s_add_i32 s10, s7, s6
	s_ashr_i32 s11, s10, 31
	s_lshl_b64 s[10:11], s[10:11], 4
	s_add_u32 s16, s24, s10
	s_addc_u32 s17, s25, s11
	global_load_dwordx4 v[40:43], v65, s[16:17]
	s_nop 0
	v_lshlrev_b32_e32 v32, 16, v92
	v_and_b32_e32 v33, 0xffff0000, v92
	v_lshlrev_b32_e32 v34, 16, v93
	v_and_b32_e32 v35, 0xffff0000, v93
	v_lshlrev_b32_e32 v92, 16, v90
	v_and_b32_e32 v93, 0xffff0000, v90
	v_lshlrev_b32_e32 v90, 16, v91
	v_and_b32_e32 v91, 0xffff0000, v91
	s_mov_b32 s16, 0x3fd744fd
	v_pk_fma_f32 v[34:35], v[34:35], s[16:17], v[90:91] op_sel_hi:[1,0,1]
	v_pk_fma_f32 v[32:33], v[32:33], s[16:17], v[92:93] op_sel_hi:[1,0,1]
	v_lshlrev_b32_e32 v90, 16, v88
	v_and_b32_e32 v91, 0xffff0000, v88
	v_lshlrev_b32_e32 v88, 16, v89
	v_and_b32_e32 v89, 0xffff0000, v89
	v_lshlrev_b32_e32 v92, 16, v86
	v_and_b32_e32 v93, 0xffff0000, v86
	v_lshlrev_b32_e32 v86, 16, v87
	v_and_b32_e32 v87, 0xffff0000, v87
	v_pk_fma_f32 v[86:87], v[88:89], s[16:17], v[86:87] op_sel_hi:[1,0,1]
	v_pk_fma_f32 v[88:89], v[90:91], s[16:17], v[92:93] op_sel_hi:[1,0,1]
	v_lshlrev_b32_e32 v90, 16, v50
	v_and_b32_e32 v91, 0xffff0000, v50
	v_lshlrev_b32_e32 v50, 16, v51
	v_and_b32_e32 v51, 0xffff0000, v51
	v_lshlrev_b32_e32 v92, 16, v48
	v_and_b32_e32 v93, 0xffff0000, v48
	v_lshlrev_b32_e32 v48, 16, v49
	v_and_b32_e32 v49, 0xffff0000, v49
	v_pk_fma_f32 v[48:49], v[50:51], s[16:17], v[48:49] op_sel_hi:[1,0,1]
	v_pk_fma_f32 v[50:51], v[90:91], s[16:17], v[92:93] op_sel_hi:[1,0,1]
	v_lshlrev_b32_e32 v90, 16, v46
	v_and_b32_e32 v91, 0xffff0000, v46
	v_lshlrev_b32_e32 v46, 16, v47
	v_and_b32_e32 v47, 0xffff0000, v47
	v_lshlrev_b32_e32 v92, 16, v44
	v_and_b32_e32 v93, 0xffff0000, v44
	v_lshlrev_b32_e32 v44, 16, v45
	v_and_b32_e32 v45, 0xffff0000, v45
	v_pk_fma_f32 v[44:45], v[46:47], s[16:17], v[44:45] op_sel_hi:[1,0,1]
	v_pk_fma_f32 v[46:47], v[90:91], s[16:17], v[92:93] op_sel_hi:[1,0,1]
	v_cvt_pk_f32_fp8_e32 v[90:91], v109
	v_cvt_pk_f32_fp8_sdwa v[92:93], v109 src0_sel:WORD_1
	v_cvt_pk_f32_fp8_e32 v[126:127], v108
	v_cvt_pk_f32_fp8_sdwa v[108:109], v108 src0_sel:WORD_1
	s_nop 0
	v_mul_f32_e32 v36, 0x3c800000, v36
	v_pk_fma_f32 v[32:33], v[36:37], v[90:91], v[32:33] op_sel_hi:[0,1,1]
	v_pk_fma_f32 v[34:35], v[36:37], v[92:93], v[34:35] op_sel_hi:[0,1,1]
	v_pk_fma_f32 v[86:87], v[36:37], v[108:109], v[86:87] op_sel_hi:[0,1,1]
	v_cvt_pk_f32_fp8_e32 v[90:91], v107
	v_cvt_pk_f32_fp8_sdwa v[92:93], v107 src0_sel:WORD_1
	v_cvt_pk_f32_fp8_e32 v[108:109], v106
	v_cvt_pk_f32_fp8_sdwa v[106:107], v106 src0_sel:WORD_1
	v_pk_fma_f32 v[50:51], v[36:37], v[90:91], v[50:51] op_sel_hi:[0,1,1]
	v_pk_fma_f32 v[48:49], v[36:37], v[92:93], v[48:49] op_sel_hi:[0,1,1]
	v_cvt_pk_f32_fp8_sdwa v[90:91], v105 src0_sel:WORD_1
	v_pk_fma_f32 v[44:45], v[36:37], v[106:107], v[44:45] op_sel_hi:[0,1,1]
	v_cvt_pk_f32_fp8_e32 v[92:93], v105
	v_cvt_pk_f32_fp8_sdwa v[106:107], v104 src0_sel:WORD_1
	v_cvt_pk_f32_fp8_e32 v[104:105], v104
	v_pk_fma_f32 v[88:89], v[36:37], v[126:127], v[88:89] op_sel_hi:[0,1,1]
	v_pk_fma_f32 v[46:47], v[36:37], v[108:109], v[46:47] op_sel_hi:[0,1,1]
	v_mul_f32_e32 v36, 0x3c800000, v37
	v_pk_fma_f32 v[34:35], v[36:37], v[90:91], v[34:35] op_sel_hi:[0,1,1]
	v_pk_fma_f32 v[32:33], v[36:37], v[92:93], v[32:33] op_sel_hi:[0,1,1]
	v_pk_fma_f32 v[88:89], v[36:37], v[104:105], v[88:89] op_sel_hi:[0,1,1]
	v_cvt_pk_f32_fp8_sdwa v[90:91], v103 src0_sel:WORD_1
	v_cvt_pk_f32_fp8_e32 v[92:93], v103
	v_cvt_pk_f32_fp8_sdwa v[104:105], v102 src0_sel:WORD_1
	v_cvt_pk_f32_fp8_e32 v[102:103], v102
	v_pk_fma_f32 v[86:87], v[36:37], v[106:107], v[86:87] op_sel_hi:[0,1,1]
	v_pk_fma_f32 v[48:49], v[36:37], v[90:91], v[48:49] op_sel_hi:[0,1,1]
	v_pk_fma_f32 v[50:51], v[36:37], v[92:93], v[50:51] op_sel_hi:[0,1,1]
	v_pk_fma_f32 v[44:45], v[36:37], v[104:105], v[44:45] op_sel_hi:[0,1,1]
	v_pk_fma_f32 v[36:37], v[36:37], v[102:103], v[46:47] op_sel_hi:[0,1,1]
	v_cvt_pk_f32_fp8_e32 v[46:47], v101
	v_cvt_pk_f32_fp8_sdwa v[90:91], v101 src0_sel:WORD_1
	v_cvt_pk_f32_fp8_e32 v[92:93], v100
	v_mul_f32_e32 v38, 0x3c800000, v38
	v_pk_fma_f32 v[32:33], v[38:39], v[46:47], v[32:33] op_sel_hi:[0,1,1]
	v_pk_fma_f32 v[34:35], v[38:39], v[90:91], v[34:35] op_sel_hi:[0,1,1]
	v_pk_fma_f32 v[46:47], v[38:39], v[92:93], v[88:89] op_sel_hi:[0,1,1]
	v_cvt_pk_f32_fp8_e32 v[88:89], v99
	v_cvt_pk_f32_fp8_sdwa v[90:91], v99 src0_sel:WORD_1
	v_cvt_pk_f32_fp8_e32 v[92:93], v98
	v_cvt_pk_f32_fp8_sdwa v[100:101], v100 src0_sel:WORD_1
	v_cvt_pk_f32_fp8_sdwa v[98:99], v98 src0_sel:WORD_1
	v_pk_fma_f32 v[50:51], v[38:39], v[88:89], v[50:51] op_sel_hi:[0,1,1]
	v_pk_fma_f32 v[48:49], v[38:39], v[90:91], v[48:49] op_sel_hi:[0,1,1]
	v_cvt_pk_f32_fp8_sdwa v[88:89], v97 src0_sel:WORD_1
	v_cvt_pk_f32_fp8_e32 v[90:91], v97
	v_pk_fma_f32 v[36:37], v[38:39], v[92:93], v[36:37] op_sel_hi:[0,1,1]
	v_cvt_pk_f32_fp8_sdwa v[92:93], v96 src0_sel:WORD_1
	v_pk_fma_f32 v[86:87], v[38:39], v[100:101], v[86:87] op_sel_hi:[0,1,1]
	v_pk_fma_f32 v[44:45], v[38:39], v[98:99], v[44:45] op_sel_hi:[0,1,1]
	v_mul_f32_e32 v38, 0x3c800000, v39
	v_cvt_pk_f32_fp8_e32 v[96:97], v96
	v_pk_fma_f32 v[88:89], v[38:39], v[88:89], v[34:35] op_sel_hi:[0,1,1]
	v_pk_fma_f32 v[90:91], v[38:39], v[90:91], v[32:33] op_sel_hi:[0,1,1]
	v_cvt_pk_f32_fp8_sdwa v[32:33], v95 src0_sel:WORD_1
	v_cvt_pk_f32_fp8_e32 v[34:35], v95
	v_pk_fma_f32 v[86:87], v[38:39], v[92:93], v[86:87] op_sel_hi:[0,1,1]
	v_cvt_pk_f32_fp8_sdwa v[92:93], v94 src0_sel:WORD_1
	v_cvt_pk_f32_fp8_e32 v[94:95], v94
	v_pk_fma_f32 v[46:47], v[38:39], v[96:97], v[46:47] op_sel_hi:[0,1,1]
	v_pk_fma_f32 v[48:49], v[38:39], v[32:33], v[48:49] op_sel_hi:[0,1,1]
	v_pk_fma_f32 v[50:51], v[38:39], v[34:35], v[50:51] op_sel_hi:[0,1,1]
	v_pk_mov_b32 v[32:33], v[90:91], v[88:89] op_sel:[1,0]
	v_mov_b32_e32 v34, v90
	v_mov_b32_e32 v35, v89
	v_pk_fma_f32 v[94:95], v[38:39], v[94:95], v[36:37] op_sel_hi:[0,1,1]
	v_pk_add_f32 v[32:33], v[32:33], v[34:35]
	v_pk_mov_b32 v[34:35], v[46:47], v[86:87] op_sel:[1,0]
	v_mov_b32_e32 v36, v46
	v_mov_b32_e32 v37, v87
	v_pk_add_f32 v[34:35], v[34:35], v[36:37]
	v_pk_fma_f32 v[92:93], v[38:39], v[92:93], v[44:45] op_sel_hi:[0,1,1]
	v_add_f32_e32 v32, v32, v33
	v_pk_add_f32 v[34:35], v[34:35], v[34:35] op_sel:[0,1] op_sel_hi:[1,0]
	v_add_f32_e32 v32, 0, v32
	v_add_f32_e32 v36, v50, v51
	v_add_f32_e32 v38, v48, v49
	v_mov_b32_e32 v33, v94
	v_mov_b32_e32 v35, v95
	v_mov_b32_e32 v37, v92
	v_mov_b32_e32 v39, v93
	v_pk_add_f32 v[32:33], v[32:33], v[34:35]
	v_pk_add_f32 v[34:35], v[36:37], v[38:39]
	s_add_u32 s10, s22, s10
	v_pk_add_f32 v[32:33], v[32:33], v[34:35]
	s_addc_u32 s11, s23, s11
	v_add_f32_e32 v32, v32, v33
	s_waitcnt vmcnt(0)
	v_readfirstlane_b32 s19, v40
	v_readfirstlane_b32 s18, v41
	v_add_f32_dpp v32, v32, v32 quad_perm:[1,0,3,2] row_mask:0xf bank_mask:0xf bound_ctrl:1
	v_readfirstlane_b32 s17, v42
	v_readfirstlane_b32 s16, v43
	v_add_f32_dpp v32, v32, v32 quad_perm:[2,3,0,1] row_mask:0xf bank_mask:0xf bound_ctrl:1
	s_nop 1
	v_add_f32_dpp v32, v32, v32 row_ror:4 row_mask:0xf bank_mask:0xf bound_ctrl:1
	s_nop 1
	v_add_f32_dpp v36, v32, v32 row_ror:8 row_mask:0xf bank_mask:0xf bound_ctrl:1
	global_load_dwordx4 v[32:35], v65, s[10:11]
	ds_swizzle_b32 v37, v36 offset:swizzle(SWAP,16)
	s_mov_b64 s[10:11], -1
	s_waitcnt lgkmcnt(0)
	v_add_f32_e32 v36, v36, v37
	v_mbcnt_lo_u32_b32 v37, -1, 0
	v_mbcnt_hi_u32_b32 v37, -1, v37
	s_nop 0
	v_lshlrev_b32_e32 v37, 2, v37
	v_xor_b32_e32 v37, 0x80, v37
	ds_bpermute_b32 v37, v37, v36
	s_waitcnt lgkmcnt(0)
	v_add_f32_e32 v98, v36, v37
	v_fmamk_f32 v91, v98, 0xba800000, v91
	v_fmac_f32_e32 v90, 0xba800000, v98
	v_fmamk_f32 v89, v98, 0xba800000, v89
	v_fmac_f32_e32 v88, 0xba800000, v98
	v_pk_mul_f32 v[36:37], v[88:89], v[88:89]
	v_pk_mul_f32 v[38:39], v[90:91], v[90:91]
	v_fmamk_f32 v47, v98, 0xba800000, v47
	v_pk_mov_b32 v[44:45], v[38:39], v[36:37] op_sel:[1,0]
	v_mov_b32_e32 v39, v37
	v_pk_add_f32 v[36:37], v[44:45], v[38:39]
	v_fmac_f32_e32 v46, 0xba800000, v98
	v_fmamk_f32 v87, v98, 0xba800000, v87
	v_fmac_f32_e32 v86, 0xba800000, v98
	v_pk_add_f32 v[36:37], v[36:37], v[36:37] op_sel_hi:[0,1]
	v_pk_mul_f32 v[38:39], v[86:87], v[86:87]
	v_pk_mul_f32 v[44:45], v[46:47], v[46:47]
	v_fmac_f32_e32 v50, 0xba800000, v98
	v_pk_mov_b32 v[96:97], v[44:45], v[38:39] op_sel:[1,0]
	v_mov_b32_e32 v45, v39
	v_fmamk_f32 v51, v98, 0xba800000, v51
	v_fmac_f32_e32 v48, 0xba800000, v98
	v_mul_f32_e32 v36, v50, v50
	v_pk_add_f32 v[38:39], v[96:97], v[44:45]
	v_fmamk_f32 v49, v98, 0xba800000, v49
	v_pk_fma_f32 v[44:45], v[50:51], v[50:51], v[36:37] op_sel_hi:[1,1,0]
	v_mul_f32_e32 v36, v48, v48
	v_pk_add_f32 v[38:39], v[38:39], v[38:39] op_sel_hi:[0,1]
	v_pk_fma_f32 v[96:97], v[48:49], v[48:49], v[36:37] op_sel_hi:[1,1,0]
	v_fmamk_f32 v93, v98, 0xba800000, v93
	v_fmac_f32_e32 v92, 0xba800000, v98
	v_fmamk_f32 v95, v98, 0xba800000, v95
	v_fmac_f32_e32 v94, 0xba800000, v98
	v_mul_f32_e32 v44, v94, v94
	v_mul_f32_e32 v96, v95, v95
	v_mul_f32_e32 v36, v92, v92
	v_mul_f32_e32 v38, v93, v93
	v_pk_add_f32 v[44:45], v[44:45], v[96:97]
	v_pk_add_f32 v[36:37], v[36:37], v[38:39]
	s_nop 0
	v_pk_add_f32 v[36:37], v[44:45], v[36:37]
	s_nop 0
	v_add_f32_e32 v36, v36, v37
	s_nop 1
	v_add_f32_dpp v36, v36, v36 quad_perm:[1,0,3,2] row_mask:0xf bank_mask:0xf bound_ctrl:1
	s_nop 1
	v_add_f32_dpp v36, v36, v36 quad_perm:[2,3,0,1] row_mask:0xf bank_mask:0xf bound_ctrl:1
	s_nop 1
	v_add_f32_dpp v36, v36, v36 row_ror:4 row_mask:0xf bank_mask:0xf bound_ctrl:1
	s_nop 1
	v_add_f32_dpp v36, v36, v36 row_ror:8 row_mask:0xf bank_mask:0xf bound_ctrl:1
	ds_swizzle_b32 v37, v36 offset:swizzle(SWAP,16)
	s_waitcnt lgkmcnt(0)
	v_add_f32_e32 v36, v36, v37
	v_mbcnt_lo_u32_b32 v37, -1, 0
	v_mbcnt_hi_u32_b32 v37, -1, v37
	s_nop 0
	v_lshlrev_b32_e32 v37, 2, v37
	v_xor_b32_e32 v37, 0x80, v37
	ds_bpermute_b32 v37, v37, v36
	s_waitcnt lgkmcnt(0)
	v_add_f32_e32 v36, v36, v37
	v_fmamk_f32 v36, v36, 0x3a800000, v218
	v_mul_f32_e32 v37, 0x4b800000, v36
	v_cmp_gt_f32_e32 vcc, s28, v36
	s_nop 1
	v_cndmask_b32_e32 v36, v36, v37, vcc
	v_rsq_f32_e32 v36, v36
	s_nop 0
	v_mul_f32_e32 v37, 0x45800000, v36
	v_cndmask_b32_e32 v96, v36, v37, vcc
	v_pk_mul_f32 v[36:37], v[90:91], v[96:97] op_sel_hi:[1,0]
	v_pk_mul_f32 v[38:39], v[88:89], v[96:97] op_sel_hi:[1,0]
	v_pk_mul_f32 v[40:41], v[46:47], v[96:97] op_sel_hi:[1,0]
	v_pk_mul_f32 v[42:43], v[86:87], v[96:97] op_sel_hi:[1,0]
	v_pk_mul_f32 v[44:45], v[50:51], v[96:97] op_sel_hi:[1,0]
	v_pk_mul_f32 v[46:47], v[48:49], v[96:97] op_sel_hi:[1,0]
	v_pk_mul_f32 v[48:49], v[94:95], v[96:97] op_sel_hi:[1,0]
	v_pk_mul_f32 v[50:51], v[92:93], v[96:97] op_sel_hi:[1,0]
	v_pk_fma_f32 v[38:39], v[2:3], v[38:39], v[6:7]
	v_pk_fma_f32 v[36:37], v[0:1], v[36:37], v[4:5]
	v_pk_fma_f32 v[42:43], v[10:11], v[42:43], v[14:15]
	v_pk_fma_f32 v[40:41], v[8:9], v[40:41], v[12:13]
	v_pk_fma_f32 v[46:47], v[18:19], v[46:47], v[22:23]
	v_pk_fma_f32 v[44:45], v[16:17], v[44:45], v[20:21]
	v_pk_fma_f32 v[50:51], v[26:27], v[50:51], v[30:31]
	v_pk_fma_f32 v[48:49], v[24:25], v[48:49], v[28:29]
	s_andn2_b64 vcc, exec, s[12:13]
	s_cbranch_vccnz .LBB0_2499
	s_ashr_i32 s7, s6, 31
	s_lshl_b64 s[38:39], s[6:7], 11
	v_lshl_add_u64 v[86:87], v[58:59], 0, s[38:39]
	v_cvt_pk_bf16_f32 v88, v36, v37
	v_cvt_pk_bf16_f32 v89, v38, v39
	global_store_dwordx2 v[86:87], v[88:89], off
	v_mul_f32_e32 v88, 0x41800000, v36
	v_mul_f32_e32 v89, 0x41800000, v37
	v_mov_b32_e32 v90, v65
	v_cvt_pk_fp8_f32 v90, v88, v89
	v_mul_f32_e32 v88, 0x41800000, v38
	v_mul_f32_e32 v89, 0x41800000, v39
	s_lshl_b64 s[10:11], s[6:7], 10
	v_cvt_pk_fp8_f32 v90, v88, v89 op_sel:[0,0,1]
	v_lshl_add_u64 v[88:89], v[62:63], 0, s[10:11]
	s_mov_b32 s7, 0x8c600000
	v_cvt_pk_bf16_f32 v91, v46, v47
	global_store_dword v[88:89], v90, off
	v_cvt_pk_bf16_f32 v88, v40, v41
	v_cvt_pk_bf16_f32 v89, v42, v43
	global_store_dwordx2 v[86:87], v[88:89], off offset:512
	v_mul_f32_e32 v88, 0x41800000, v40
	v_mul_f32_e32 v89, 0x41800000, v41
	v_mov_b32_e32 v90, v65
	v_cvt_pk_fp8_f32 v90, v88, v89
	v_mul_f32_e32 v88, 0x41800000, v42
	v_mul_f32_e32 v89, 0x41800000, v43
	v_mov_b32_e32 v92, v65
	v_cvt_pk_fp8_f32 v90, v88, v89 op_sel:[0,0,1]
	v_lshl_add_u64 v[88:89], v[60:61], 0, s[10:11]
	v_add_co_u32_e32 v88, vcc, s7, v88
	s_mov_b64 s[10:11], 0
	s_nop 0
	v_addc_co_u32_e32 v89, vcc, 0, v89, vcc
	global_store_dword v[88:89], v90, off offset:256
	v_cvt_pk_bf16_f32 v90, v44, v45
	global_store_dwordx2 v[86:87], v[90:91], off offset:1024
	v_mul_f32_e32 v90, 0x41800000, v44
	v_mul_f32_e32 v91, 0x41800000, v45
	v_cvt_pk_fp8_f32 v92, v90, v91
	v_mul_f32_e32 v90, 0x41800000, v46
	v_mul_f32_e32 v91, 0x41800000, v47
	v_cvt_pk_fp8_f32 v92, v90, v91 op_sel:[0,0,1]
	v_cvt_pk_bf16_f32 v90, v48, v49
	v_cvt_pk_bf16_f32 v91, v50, v51
	global_store_dword v[88:89], v92, off offset:512
	global_store_dwordx2 v[86:87], v[90:91], off offset:1536
	v_mul_f32_e32 v86, 0x41800000, v48
	v_mul_f32_e32 v87, 0x41800000, v49
	v_mov_b32_e32 v90, v65
	v_cvt_pk_fp8_f32 v90, v86, v87
	v_mul_f32_e32 v86, 0x41800000, v50
	v_mul_f32_e32 v87, 0x41800000, v51
	v_cvt_pk_fp8_f32 v90, v86, v87 op_sel:[0,0,1]
	global_store_dword v[88:89], v90, off offset:768
